# gain-load ladders hoisted out of the P0 rmsnorm(x) and P12 combine row loops; P8: the 8 D7 row loads issued together with counted vmcnt(7)
# speedup vs baseline: 1.0189x; 1.0189x over previous
; __device__ __forceinline__ unsigned cvt4_fp8(float a, float b, float c, float d) { int w = 0; w = __builtin_amdgcn_cvt_pk_fp8_f32(a, b, w, false); w = __builtin_amdgcn_cvt_pk_fp8_f32(c, d, w, true); return (unsigned)w; }
; __global__ void __launch_bounds__(512, 2) mega_fwd(Args args) {
;     ...
;         { const float* gn = args.in[I_ATTN_NORM];
;           for (int m = gwc; m < T; m += NGWc) { const f32x4* xr = (const f32x4*)(x + (size_t)m * DM) + lane; f32x4 v[8]; float s = 0.f;
; #pragma unroll
;               for (int j = 0; j < 8; ++j) { v[j] = xr[64 * j]; s += (v[j][0] * v[j][0] + v[j][1] * v[j][1]) + (v[j][2] * v[j][2] + v[j][3] * v[j][3]); }
;               const float rstd = 1.0f / sqrtf(wave_sum(s) * (1.0f / DM) + EPS);
;               unsigned* o4 = (unsigned*)(XN8 + (size_t)m * DM) + lane;
; #pragma unroll
;               for (int j = 0; j < 8; ++j) { const f32x4 gv = ((const f32x4*)gn)[64 * j + lane]; o4[64 * j] = cvt4_fp8(v[j][0] * rstd * gv[0], v[j][1] * rstd * gv[1], v[j][2] * rstd * gv[2], v[j][3] * rstd * gv[3]); } } }
.LBB0_1091:
	s_or_b64 exec, exec, s[4:5]
	s_load_dwordx4 s[8:11], s[0:1], 0x8
	s_load_dwordx2 s[46:47], s[0:1], 0x68
	s_cmpk_gt_i32 s42, 0x3fff
	s_cbranch_scc1 .LBB0_1094
	v_mbcnt_lo_u32_b32 v2, -1, 0
	v_mbcnt_hi_u32_b32 v2, -1, v2
	v_and_b32_e32 v3, 64, v2
	v_add_u32_e32 v3, 64, v3
	v_xor_b32_e32 v4, 1, v2
	v_cmp_lt_i32_e32 vcc, v4, v3
	s_load_dwordx2 s[16:17], s[0:1], 0x0
	s_ashr_i32 s43, s42, 31
	v_cndmask_b32_e32 v4, v2, v4, vcc
	v_lshlrev_b32_e32 v38, 2, v4
	v_xor_b32_e32 v4, 2, v2
	v_cmp_lt_i32_e32 vcc, v4, v3
	s_mov_b64 s[4:5], 0x1000
	v_mov_b32_e32 v44, 0x358637bd
	v_cndmask_b32_e32 v4, v2, v4, vcc
	v_lshlrev_b32_e32 v39, 2, v4
	v_xor_b32_e32 v4, 4, v2
	v_cmp_lt_i32_e32 vcc, v4, v3
	s_mov_b32 s3, 0xf800000
	v_mov_b32_e32 v45, 0x260
	v_cndmask_b32_e32 v4, v2, v4, vcc
	v_lshlrev_b32_e32 v40, 2, v4
	v_xor_b32_e32 v4, 8, v2
	v_cmp_lt_i32_e32 vcc, v4, v3
	s_nop 1
	v_cndmask_b32_e32 v4, v2, v4, vcc
	v_lshlrev_b32_e32 v41, 2, v4
	v_xor_b32_e32 v4, 16, v2
	v_cmp_lt_i32_e32 vcc, v4, v3
	s_nop 1
	v_cndmask_b32_e32 v4, v2, v4, vcc
	v_lshlrev_b32_e32 v42, 2, v4
	v_xor_b32_e32 v4, 32, v2
	v_cmp_lt_i32_e32 vcc, v4, v3
	v_mov_b32_e32 v3, 0
	s_nop 0
	v_cndmask_b32_e32 v2, v2, v4, vcc
	v_lshlrev_b32_e32 v43, 2, v2
	v_lshlrev_b32_e32 v2, 4, v164
	s_waitcnt lgkmcnt(0)
	v_lshl_add_u64 v[24:25], s[10:11], 0, v[2:3]
	s_mov_b64 s[10:11], 0x1400
	s_waitcnt vmcnt(0)
	v_lshl_add_u64 v[28:29], v[24:25], 0, s[10:11]
	s_mov_b64 s[10:11], 0x1800
	v_lshl_add_u64 v[30:31], v[24:25], 0, s[10:11]
	s_mov_b64 s[10:11], 0x1c00
	v_lshl_add_u64 v[32:33], v[24:25], 0, s[10:11]
	s_lshl_b64 s[10:11], s[42:43], 13
	s_add_u32 s10, s16, s10
	s_addc_u32 s11, s17, s11
	v_lshl_add_u64 v[4:5], s[10:11], 0, v[2:3]
	s_ashr_i32 s45, s44, 31
	v_lshl_add_u64 v[26:27], v[24:25], 0, s[4:5]
	v_lshl_add_u64 v[34:35], v[4:5], 0, s[4:5]
	s_lshl_b64 s[10:11], s[44:45], 13
	s_lshl_b64 s[4:5], s[42:43], 11
	s_add_u32 s4, s18, s4
	v_lshlrev_b32_e32 v2, 2, v164
	s_addc_u32 s5, s19, s5
	v_lshl_add_u64 v[2:3], s[4:5], 0, v[2:3]
	s_mov_b64 s[4:5], 0x25000000
	v_lshl_add_u64 v[36:37], v[2:3], 0, s[4:5]
	s_lshl_b64 s[48:49], s[44:45], 11
	global_load_dwordx4 v[200:203], v[24:25], off offset:1024
	global_load_dwordx4 v[204:207], v[24:25], off offset:2048
	global_load_dwordx4 v[208:211], v[24:25], off offset:3072
	global_load_dwordx4 v[212:215], v[26:27], off
	global_load_dwordx4 v[216:219], v[28:29], off
	global_load_dwordx4 v[220:223], v[30:31], off
	global_load_dwordx4 v[224:227], v[32:33], off
	s_waitcnt vmcnt(0)
.LBB0_1093:
	global_load_dwordx4 v[46:49], v[34:35], off offset:-4096
	global_load_dwordx4 v[50:53], v[34:35], off offset:-3072
	global_load_dwordx4 v[54:57], v[34:35], off offset:-2048
	global_load_dwordx4 v[18:21], v[34:35], off offset:-1024
	global_load_dwordx4 v[14:17], v[34:35], off
	global_load_dwordx4 v[10:13], v[34:35], off offset:1024
	global_load_dwordx4 v[6:9], v[34:35], off offset:2048
	global_load_dwordx4 v[2:5], v[34:35], off offset:3072
	global_load_dwordx4 v[58:61], v[24:25], off
	v_mov_b32_e32 v62, 0
	s_add_i32 s42, s42, s44
	v_lshl_add_u64 v[34:35], v[34:35], 0, s[10:11]
	s_cmpk_gt_i32 s42, 0x3fff
	s_waitcnt vmcnt(8)
	v_mul_f32_e32 v63, v47, v47
	v_mul_f32_e32 v64, v49, v49
	s_waitcnt vmcnt(7)
	v_mul_f32_e32 v65, v51, v51
	v_mul_f32_e32 v66, v53, v53
	s_waitcnt vmcnt(6)
	v_mul_f32_e32 v67, v55, v55
	v_mul_f32_e32 v68, v57, v57
	v_fmac_f32_e32 v63, v46, v46
	v_fmac_f32_e32 v64, v48, v48
	v_fmac_f32_e32 v65, v50, v50
	v_fmac_f32_e32 v66, v52, v52
	s_waitcnt vmcnt(5)
	v_mul_f32_e32 v69, v19, v19
	v_mul_f32_e32 v70, v21, v21
	v_fmac_f32_e32 v67, v54, v54
	v_fmac_f32_e32 v68, v56, v56
	v_add_f32_e32 v63, v63, v64
	v_add_f32_e32 v64, v65, v66
	s_waitcnt vmcnt(4)
	v_mul_f32_e32 v71, v15, v15
	v_mul_f32_e32 v72, v17, v17
	v_fmac_f32_e32 v69, v18, v18
	v_fmac_f32_e32 v70, v20, v20
	v_add_f32_e32 v65, v67, v68
	v_add_f32_e32 v63, v63, v64
	s_waitcnt vmcnt(3)
	v_mul_f32_e32 v73, v11, v11
	v_mul_f32_e32 v74, v13, v13
	v_fmac_f32_e32 v71, v14, v14
	v_fmac_f32_e32 v72, v16, v16
	v_add_f32_e32 v66, v69, v70
	v_add_f32_e32 v63, v63, v65
	s_waitcnt vmcnt(2)
	v_mul_f32_e32 v75, v7, v7
	v_mul_f32_e32 v76, v9, v9
	v_fmac_f32_e32 v73, v10, v10
	v_fmac_f32_e32 v74, v12, v12
	v_add_f32_e32 v67, v71, v72
	v_add_f32_e32 v63, v63, v66
	s_waitcnt vmcnt(1)
	v_mul_f32_e32 v77, v3, v3
	v_mul_f32_e32 v78, v5, v5
	v_fmac_f32_e32 v75, v6, v6
	v_fmac_f32_e32 v76, v8, v8
	v_add_f32_e32 v68, v73, v74
	v_add_f32_e32 v63, v63, v67
	v_fmac_f32_e32 v77, v2, v2
	v_fmac_f32_e32 v78, v4, v4
	v_add_f32_e32 v69, v75, v76
	v_add_f32_e32 v63, v63, v68
	v_add_f32_e32 v70, v77, v78
	v_add_f32_e32 v63, v63, v69
	v_add_f32_e32 v63, v63, v70
	ds_bpermute_b32 v64, v38, v63
	s_waitcnt lgkmcnt(0)
	v_add_f32_e32 v63, v63, v64
	ds_bpermute_b32 v64, v39, v63
	s_waitcnt lgkmcnt(0)
	v_add_f32_e32 v63, v63, v64
	ds_bpermute_b32 v64, v40, v63
	s_waitcnt lgkmcnt(0)
	v_add_f32_e32 v63, v63, v64
	ds_bpermute_b32 v64, v41, v63
	s_waitcnt lgkmcnt(0)
; __device__ __forceinline__ unsigned cvt4_fp8(float a, float b, float c, float d) { int w = 0; w = __builtin_amdgcn_cvt_pk_fp8_f32(a, b, w, false); w = __builtin_amdgcn_cvt_pk_fp8_f32(c, d, w, true); return (unsigned)w; }
; __global__ void __launch_bounds__(512, 2) mega_fwd(Args args) {
;     ...
;               for (int j = 0; j < 8; ++j) { v[j] = xr[64 * j]; s += (v[j][0] * v[j][0] + v[j][1] * v[j][1]) + (v[j][2] * v[j][2] + v[j][3] * v[j][3]); }
;               const float rstd = 1.0f / sqrtf(wave_sum(s) * (1.0f / DM) + EPS);
;               unsigned* o4 = (unsigned*)(XN8 + (size_t)m * DM) + lane;
; #pragma unroll
;               for (int j = 0; j < 8; ++j) { const f32x4 gv = ((const f32x4*)gn)[64 * j + lane]; o4[64 * j] = cvt4_fp8(v[j][0] * rstd * gv[0], v[j][1] * rstd * gv[1], v[j][2] * rstd * gv[2], v[j][3] * rstd * gv[3]); } } }
	v_add_f32_e32 v63, v63, v64
	ds_bpermute_b32 v64, v42, v63
	s_waitcnt lgkmcnt(0)
	v_add_f32_e32 v63, v63, v64
	ds_bpermute_b32 v64, v43, v63
	s_waitcnt lgkmcnt(0)
	v_add_f32_e32 v63, v63, v64
	v_fmamk_f32 v63, v63, 0x3a000000, v44
	v_mul_f32_e32 v64, 0x4f800000, v63
	v_cmp_gt_f32_e32 vcc, s3, v63
	s_nop 1
	v_cndmask_b32_e32 v63, v63, v64, vcc
	v_sqrt_f32_e32 v64, v63
	s_nop 0
	v_add_u32_e32 v65, -1, v64
	v_add_u32_e32 v66, 1, v64
	v_fma_f32 v67, -v65, v64, v63
	v_fma_f32 v68, -v66, v64, v63
	v_cmp_ge_f32_e64 s[4:5], 0, v67
	s_nop 1
	v_cndmask_b32_e64 v64, v64, v65, s[4:5]
	v_cmp_lt_f32_e64 s[4:5], 0, v68
	s_nop 1
	v_cndmask_b32_e64 v64, v64, v66, s[4:5]
	v_mul_f32_e32 v65, 0x37800000, v64
	v_cndmask_b32_e32 v64, v64, v65, vcc
	v_cmp_class_f32_e32 vcc, v63, v45
	s_nop 1
	v_cndmask_b32_e32 v63, v64, v63, vcc
	v_div_scale_f32 v64, s[4:5], v63, v63, 1.0
	v_rcp_f32_e32 v66, v64
	v_div_scale_f32 v65, vcc, 1.0, v63, 1.0
	v_fma_f32 v67, -v64, v66, 1.0
	v_fmac_f32_e32 v66, v67, v66
	v_mul_f32_e32 v67, v65, v66
	v_fma_f32 v68, -v64, v67, v65
	v_fmac_f32_e32 v67, v68, v66
	v_fma_f32 v64, -v64, v67, v65
	v_div_fmas_f32 v64, v64, v66, v67
	v_div_fixup_f32 v63, v64, v63, 1.0
	v_mul_f32_e32 v46, v63, v46
	v_mul_f32_e32 v47, v63, v47
	s_waitcnt vmcnt(0)
	v_mul_f32_e32 v46, v58, v46
	v_mul_f32_e32 v47, v59, v47
	v_cvt_pk_fp8_f32 v62, v46, v47
	v_mul_f32_e32 v48, v63, v48
	v_mul_f32_e32 v49, v63, v49
	v_mul_f32_e32 v48, v60, v48
	v_mul_f32_e32 v49, v61, v49
	v_cvt_pk_fp8_f32 v62, v48, v49 op_sel:[0,0,1]
	v_mul_f32_e32 v50, v63, v50
	v_mul_f32_e32 v51, v63, v51
	v_mov_b32_e32 v58, 0
	global_store_dword v[36:37], v62, off
	v_mul_f32_e32 v52, v63, v52
	v_mul_f32_e32 v53, v63, v53
	v_mul_f32_e32 v18, v63, v18
	v_mul_f32_e32 v19, v63, v19
	v_mul_f32_e32 v20, v63, v20
	v_mul_f32_e32 v21, v63, v21
	v_mul_f32_e32 v14, v63, v14
	v_mul_f32_e32 v15, v63, v15
	v_mul_f32_e32 v16, v63, v16
	v_mul_f32_e32 v17, v63, v17
	v_mul_f32_e32 v10, v63, v10
	v_mul_f32_e32 v11, v63, v11
	v_mul_f32_e32 v12, v63, v12
	v_mul_f32_e32 v13, v63, v13
	v_mul_f32_e32 v6, v63, v6
	v_mul_f32_e32 v7, v63, v7
	v_mul_f32_e32 v8, v63, v8
	v_mul_f32_e32 v9, v63, v9
	v_mul_f32_e32 v2, v63, v2
	v_mul_f32_e32 v3, v63, v3
	v_mul_f32_e32 v4, v63, v4
	v_mul_f32_e32 v5, v63, v5
	v_mov_b32_e32 v46, v200
	v_mov_b32_e32 v47, v201
	v_mov_b32_e32 v48, v202
	v_mov_b32_e32 v49, v203
	v_mul_f32_e32 v46, v46, v50
	v_mul_f32_e32 v47, v47, v51
	v_cvt_pk_fp8_f32 v58, v46, v47
	v_mul_f32_e32 v48, v48, v52
	v_mul_f32_e32 v49, v49, v53
	v_mul_f32_e32 v51, v63, v54
	v_cvt_pk_fp8_f32 v58, v48, v49 op_sel:[0,0,1]
	v_mul_f32_e32 v52, v63, v55
	v_mov_b32_e32 v50, 0
	v_mul_f32_e32 v53, v63, v56
	global_store_dword v[36:37], v58, off offset:256
	v_mul_f32_e32 v54, v63, v57
	v_mov_b32_e32 v46, v204
	v_mov_b32_e32 v47, v205
	v_mov_b32_e32 v48, v206
	v_mov_b32_e32 v49, v207
	v_mul_f32_e32 v46, v46, v51
	v_mul_f32_e32 v47, v47, v52
	v_cvt_pk_fp8_f32 v50, v46, v47
	v_mul_f32_e32 v48, v48, v53
	v_mul_f32_e32 v49, v49, v54
	v_cvt_pk_fp8_f32 v50, v48, v49 op_sel:[0,0,1]
	global_store_dword v[36:37], v50, off offset:512
	v_mov_b32_e32 v50, 0
	v_mov_b32_e32 v46, v208
	v_mov_b32_e32 v47, v209
	v_mov_b32_e32 v48, v210
	v_mov_b32_e32 v49, v211
	v_mul_f32_e32 v18, v46, v18
	v_mul_f32_e32 v19, v47, v19
	v_cvt_pk_fp8_f32 v50, v18, v19
	v_mul_f32_e32 v20, v48, v20
	v_mul_f32_e32 v21, v49, v21
	v_mov_b32_e32 v46, 0
	v_cvt_pk_fp8_f32 v50, v20, v21 op_sel:[0,0,1]
	global_store_dword v[36:37], v50, off offset:768
	v_mov_b32_e32 v18, v212
	v_mov_b32_e32 v19, v213
	v_mov_b32_e32 v20, v214
	v_mov_b32_e32 v21, v215
	v_mul_f32_e32 v14, v18, v14
	v_mul_f32_e32 v15, v19, v15
	v_cvt_pk_fp8_f32 v46, v14, v15
	v_mul_f32_e32 v16, v20, v16
	v_mul_f32_e32 v17, v21, v17
	v_mov_b32_e32 v18, 0
	v_cvt_pk_fp8_f32 v46, v16, v17 op_sel:[0,0,1]
	global_store_dword v[36:37], v46, off offset:1024
	v_mov_b32_e32 v14, v216
	v_mov_b32_e32 v15, v217
	v_mov_b32_e32 v16, v218
	v_mov_b32_e32 v17, v219
	v_mul_f32_e32 v10, v14, v10
	v_mul_f32_e32 v11, v15, v11
	v_cvt_pk_fp8_f32 v18, v10, v11
	v_mul_f32_e32 v12, v16, v12
	v_mul_f32_e32 v13, v17, v13
	v_mov_b32_e32 v14, 0
	v_cvt_pk_fp8_f32 v18, v12, v13 op_sel:[0,0,1]
	global_store_dword v[36:37], v18, off offset:1280
	v_mov_b32_e32 v10, v220
	v_mov_b32_e32 v11, v221
	v_mov_b32_e32 v12, v222
	v_mov_b32_e32 v13, v223
	v_mul_f32_e32 v6, v10, v6
	v_mul_f32_e32 v7, v11, v7
	v_cvt_pk_fp8_f32 v14, v6, v7
	v_mul_f32_e32 v8, v12, v8
	v_mul_f32_e32 v6, v13, v9
	v_mov_b32_e32 v10, 0
	v_cvt_pk_fp8_f32 v14, v8, v6 op_sel:[0,0,1]
	global_store_dword v[36:37], v14, off offset:1536
	v_mov_b32_e32 v6, v224
	v_mov_b32_e32 v7, v225
	v_mov_b32_e32 v8, v226
	v_mov_b32_e32 v9, v227
	v_mul_f32_e32 v2, v6, v2
	v_mul_f32_e32 v3, v7, v3
	v_cvt_pk_fp8_f32 v10, v2, v3
	v_mul_f32_e32 v2, v8, v4
	v_mul_f32_e32 v3, v9, v5
	v_cvt_pk_fp8_f32 v10, v2, v3 op_sel:[0,0,1]
	global_store_dword v[36:37], v10, off offset:1792
	v_lshl_add_u64 v[36:37], v[36:37], 0, s[48:49]
	s_cbranch_scc0 .LBB0_1093

; __device__ __forceinline__ unsigned cvtpk(float lo, float hi) { unsigned r; asm volatile("v_cvt_pk_bf16_f32 %0, %1, %2" : "=v"(r) : "v"(lo), "v"(hi)); return r; }
; __device__ __forceinline__ float bflo(unsigned w) { return __uint_as_float(w << 16); }
; __device__ __forceinline__ float bfhi(unsigned w) { return __uint_as_float(w & 0xffff0000u); }
; __global__ void __launch_bounds__(512, 2) mega_fwd(Args args) {
;     ...
;             for (int r = 0; r < RPW; ++r) { const int rowc = wave * RPW + r, m = ch * CR + rowc; float ssq = 0.f;
;                 { const u32x2* dr = (const u32x2*)(D7 + (size_t)m * DM) + lane; u32x2* hr = (u32x2*)(H1 + (size_t)m * DM) + lane;
; #pragma unroll
;                   for (int j = 0; j < 8; ++j) { const u32x2 d = dr[64 * j]; nv[r][j][0] += bflo(d.x); nv[r][j][1] += bfhi(d.x); nv[r][j][2] += bflo(d.y); nv[r][j][3] += bfhi(d.y); u32x2 hw_; hw_.x = cvtpk(nv[r][j][0], nv[r][j][1]); hw_.y = cvtpk(nv[r][j][2], nv[r][j][3]); hr[64 * j] = hw_; } }
; #pragma unroll
;                 for (int j = 0; j < 8; ++j) ssq += (nv[r][j][0] * nv[r][j][0] + nv[r][j][1] * nv[r][j][1]) + (nv[r][j][2] * nv[r][j][2] + nv[r][j][3] * nv[r][j][3]);
.LBB0_1996:
	s_add_i32 s52, s74, s3
	s_ashr_i32 s53, s52, 31
	s_lshl_b64 s[16:17], s[52:53], 12
	v_lshl_add_u64 v[194:195], v[168:169], 0, s[16:17]
	global_load_dwordx2 v[232:233], v[194:195], off
	global_load_dwordx2 v[234:235], v[194:195], off offset:512
	global_load_dwordx2 v[236:237], v[194:195], off offset:1024
	global_load_dwordx2 v[238:239], v[194:195], off offset:1536
	global_load_dwordx2 v[240:241], v[194:195], off offset:2048
	global_load_dwordx2 v[242:243], v[194:195], off offset:2560
	global_load_dwordx2 v[244:245], v[194:195], off offset:3072
	global_load_dwordx2 v[246:247], v[194:195], off offset:3584
	v_and_b32_e32 v191, 64, v206
	v_add_u32_e32 v224, 64, v191
	s_add_i32 s55, s55, s82
	v_add_u32_e32 v225, s27, v200
	s_waitcnt vmcnt(7)
	v_mov_b32_e32 v192, v232
	v_mov_b32_e32 v193, v233
	v_lshlrev_b32_e32 v208, 16, v192
	v_and_b32_e32 v209, 0xffff0000, v192
	v_lshlrev_b32_e32 v192, 16, v193
	v_and_b32_e32 v193, 0xffff0000, v193
	v_pk_add_f32 v[130:131], v[130:131], v[208:209]
	v_pk_add_f32 v[132:133], v[132:133], v[192:193]
	v_cvt_pk_bf16_f32 v208, v130, v131
	v_lshl_add_u64 v[192:193], v[170:171], 0, s[16:17]
	v_cvt_pk_bf16_f32 v209, v132, v133
	v_mov_b32_e32 v212, v131
	global_store_dwordx2 v[192:193], v[208:209], off
	v_mov_b32_e32 v216, v133
	v_mov_b32_e32 v214, v132
	s_waitcnt vmcnt(7)
	v_mov_b32_e32 v210, v234
	v_mov_b32_e32 v211, v235
	v_lshlrev_b32_e32 v208, 16, v210
	v_and_b32_e32 v209, 0xffff0000, v210
	v_lshlrev_b32_e32 v210, 16, v211
	v_and_b32_e32 v211, 0xffff0000, v211
	v_pk_add_f32 v[134:135], v[134:135], v[208:209]
	v_pk_add_f32 v[136:137], v[136:137], v[210:211]
	v_cvt_pk_bf16_f32 v208, v134, v135
	v_mov_b32_e32 v213, v135
	v_cvt_pk_bf16_f32 v209, v136, v137
	v_mov_b32_e32 v217, v137
	global_store_dwordx2 v[192:193], v[208:209], off offset:512
	v_mov_b32_e32 v215, v136
	v_pk_mul_f32 v[212:213], v[212:213], v[212:213]
	v_pk_mul_f32 v[216:217], v[216:217], v[216:217]
	s_waitcnt vmcnt(7)
	v_mov_b32_e32 v210, v236
	v_mov_b32_e32 v211, v237
	v_lshlrev_b32_e32 v208, 16, v210
	v_and_b32_e32 v209, 0xffff0000, v210
	v_lshlrev_b32_e32 v210, 16, v211
	v_and_b32_e32 v211, 0xffff0000, v211
	v_pk_add_f32 v[138:139], v[138:139], v[208:209]
	v_pk_add_f32 v[140:141], v[140:141], v[210:211]
	v_cvt_pk_bf16_f32 v208, v138, v139
	s_nop 0
	v_cvt_pk_bf16_f32 v209, v140, v141
	s_nop 0
	global_store_dwordx2 v[192:193], v[208:209], off offset:1024
	s_waitcnt vmcnt(7)
	v_mov_b32_e32 v210, v238
	v_mov_b32_e32 v211, v239
	v_lshlrev_b32_e32 v208, 16, v210
	v_and_b32_e32 v209, 0xffff0000, v210
	v_lshlrev_b32_e32 v210, 16, v211
	v_and_b32_e32 v211, 0xffff0000, v211
	v_pk_add_f32 v[142:143], v[142:143], v[208:209]
	v_pk_add_f32 v[144:145], v[144:145], v[210:211]
	v_cvt_pk_bf16_f32 v208, v142, v143
	s_nop 0
	v_cvt_pk_bf16_f32 v209, v144, v145
	s_nop 0
	global_store_dwordx2 v[192:193], v[208:209], off offset:1536
	s_waitcnt vmcnt(7)
	v_mov_b32_e32 v210, v240
	v_mov_b32_e32 v211, v241
	v_lshlrev_b32_e32 v208, 16, v210
	v_and_b32_e32 v209, 0xffff0000, v210
	v_lshlrev_b32_e32 v210, 16, v211
	v_and_b32_e32 v211, 0xffff0000, v211
	v_pk_add_f32 v[146:147], v[146:147], v[208:209]
	v_pk_add_f32 v[148:149], v[148:149], v[210:211]
	v_cvt_pk_bf16_f32 v208, v146, v147
	v_pk_mul_f32 v[218:219], v[146:147], v[146:147]
	v_cvt_pk_bf16_f32 v209, v148, v149
	v_pk_mul_f32 v[220:221], v[148:149], v[148:149]
	global_store_dwordx2 v[192:193], v[208:209], off offset:2048
	s_waitcnt vmcnt(7)
	v_mov_b32_e32 v210, v242
	v_mov_b32_e32 v211, v243
	v_lshlrev_b32_e32 v208, 16, v210
	v_and_b32_e32 v209, 0xffff0000, v210
	v_lshlrev_b32_e32 v210, 16, v211
	v_and_b32_e32 v211, 0xffff0000, v211
	v_pk_add_f32 v[150:151], v[150:151], v[208:209]
	v_pk_add_f32 v[152:153], v[152:153], v[210:211]
	v_cvt_pk_bf16_f32 v208, v150, v151
	s_nop 0
	v_cvt_pk_bf16_f32 v209, v152, v153
	s_nop 0
	global_store_dwordx2 v[192:193], v[208:209], off offset:2560
	s_waitcnt vmcnt(7)
	v_mov_b32_e32 v210, v244
	v_mov_b32_e32 v211, v245
	v_lshlrev_b32_e32 v208, 16, v210
	v_and_b32_e32 v209, 0xffff0000, v210
	v_lshlrev_b32_e32 v210, 16, v211
	v_and_b32_e32 v211, 0xffff0000, v211
	v_pk_add_f32 v[154:155], v[154:155], v[208:209]
	v_pk_add_f32 v[156:157], v[156:157], v[210:211]
	v_cvt_pk_bf16_f32 v208, v154, v155
	v_xor_b32_e32 v210, 1, v206
	v_cvt_pk_bf16_f32 v209, v156, v157
	v_cmp_lt_i32_e32 vcc, v210, v224
	v_mov_b32_e32 v211, v134
	global_store_dwordx2 v[192:193], v[208:209], off offset:3072
	v_cndmask_b32_e32 v191, v206, v210, vcc
	v_mov_b32_e32 v210, v130
	v_pk_fma_f32 v[210:211], v[210:211], v[210:211], v[212:213]
	v_pk_fma_f32 v[212:213], v[214:215], v[214:215], v[216:217]
	v_mov_b32_e32 v214, v139
	v_mov_b32_e32 v215, v141
	v_pk_add_f32 v[210:211], v[210:211], v[212:213]
	v_mov_b32_e32 v212, v138
	v_mov_b32_e32 v213, v140
	v_pk_mul_f32 v[214:215], v[214:215], v[214:215]
	v_mul_f32_e32 v216, v145, v145
	v_pk_fma_f32 v[212:213], v[212:213], v[212:213], v[214:215]
	v_mul_f32_e32 v214, v143, v143
	v_pk_add_f32 v[210:211], v[210:211], v[210:211] op_sel:[0,1] op_sel_hi:[1,0]
	v_pk_add_f32 v[212:213], v[212:213], v[212:213] op_sel:[0,1] op_sel_hi:[1,0]
	v_pk_fma_f32 v[214:215], v[142:143], v[142:143], v[214:215] op_sel_hi:[1,1,0]
	v_pk_fma_f32 v[216:217], v[144:145], v[144:145], v[216:217] op_sel_hi:[1,1,0]
	v_mov_b32_e32 v211, v218
	v_mov_b32_e32 v213, v219
	v_mov_b32_e32 v215, v220
	v_mov_b32_e32 v217, v221
	v_pk_add_f32 v[210:211], v[210:211], v[212:213]
	v_pk_add_f32 v[212:213], v[214:215], v[216:217]
	v_mov_b32_e32 v214, v151
	v_mov_b32_e32 v215, v153
	v_pk_add_f32 v[210:211], v[210:211], v[212:213]
	v_mov_b32_e32 v212, v150
	v_mov_b32_e32 v213, v152
	v_pk_mul_f32 v[214:215], v[214:215], v[214:215]
	v_pk_add_f32 v[210:211], v[210:211], v[210:211] op_sel:[0,1] op_sel_hi:[1,0]
	v_pk_fma_f32 v[212:213], v[212:213], v[212:213], v[214:215]
	v_mul_f32_e32 v214, v157, v157
	v_pk_add_f32 v[216:217], v[212:213], v[212:213] op_sel:[0,1] op_sel_hi:[1,0]
	v_mul_f32_e32 v212, v155, v155
	v_pk_fma_f32 v[208:209], v[154:155], v[154:155], v[212:213] op_sel_hi:[1,1,0]
	v_pk_fma_f32 v[218:219], v[156:157], v[156:157], v[214:215] op_sel_hi:[1,1,0]
	v_lshlrev_b32_e32 v191, 2, v191
	s_waitcnt vmcnt(7)
; #define LAS __attribute__((address_space(3)))
; __device__ __forceinline__ unsigned cvtpk(float lo, float hi) { unsigned r; asm volatile("v_cvt_pk_bf16_f32 %0, %1, %2" : "=v"(r) : "v"(lo), "v"(hi)); return r; }
; __device__ __forceinline__ unsigned cvt4_fp8(float a, float b, float c, float d) { int w = 0; w = __builtin_amdgcn_cvt_pk_fp8_f32(a, b, w, false); w = __builtin_amdgcn_cvt_pk_fp8_f32(c, d, w, true); return (unsigned)w; }
; __device__ __forceinline__ float bflo(unsigned w) { return __uint_as_float(w << 16); }
; __device__ __forceinline__ float bfhi(unsigned w) { return __uint_as_float(w & 0xffff0000u); }
; __global__ void __launch_bounds__(512, 2) mega_fwd(Args args) {
;     ...
;                   for (int j = 0; j < 8; ++j) { const u32x2 d = dr[64 * j]; nv[r][j][0] += bflo(d.x); nv[r][j][1] += bfhi(d.x); nv[r][j][2] += bflo(d.y); nv[r][j][3] += bfhi(d.y); u32x2 hw_; hw_.x = cvtpk(nv[r][j][0], nv[r][j][1]); hw_.y = cvtpk(nv[r][j][2], nv[r][j][3]); hr[64 * j] = hw_; } }
; #pragma unroll
;                 for (int j = 0; j < 8; ++j) ssq += (nv[r][j][0] * nv[r][j][0] + nv[r][j][1] * nv[r][j][1]) + (nv[r][j][2] * nv[r][j][2] + nv[r][j][3] * nv[r][j][3]);
;                 const float rstd = 1.0f / sqrtf(wave_sum(ssq) * (1.0f / DM) + EPS);
;                 unsigned* o4 = (unsigned*)(XN8 + (size_t)m * DM) + lane;
; #pragma unroll
;                 for (int j = 0; j < 8; ++j) { const f32x4 gv = ((const f32x4*)gn)[64 * j + lane]; const f32x4 y = nv[r][j] * rstd * gv;
;                     o4[64 * j] = cvt4_fp8(y[0], y[1], y[2], y[3]);
;                     u32x2 hw, lw; hw.x = cvtpk(y[0], y[1]); hw.y = cvtpk(y[2], y[3]);
;                     lw.x = cvtpk(y[0] - bflo(hw.x), y[1] - bfhi(hw.x)); lw.y = cvtpk(y[2] - bflo(hw.y), y[3] - bfhi(hw.y));
;                     *(LAS u32x2*)(Ahi + rowc * AST + (64 * j + lane) * 8) = hw; *(LAS u32x2*)(Alo + rowc * AST + (64 * j + lane) * 8) = lw; } }
	v_mov_b32_e32 v194, v246
	v_mov_b32_e32 v195, v247
	v_lshlrev_b32_e32 v212, 16, v194
	v_and_b32_e32 v213, 0xffff0000, v194
	v_lshlrev_b32_e32 v194, 16, v195
	v_and_b32_e32 v195, 0xffff0000, v195
	v_pk_add_f32 v[158:159], v[158:159], v[212:213]
	v_pk_add_f32 v[160:161], v[160:161], v[194:195]
	v_cvt_pk_bf16_f32 v194, v158, v159
	v_pk_mul_f32 v[220:221], v[158:159], v[158:159]
	v_cvt_pk_bf16_f32 v195, v160, v161
	global_store_dwordx2 v[192:193], v[194:195], off offset:3584
	global_load_dwordx4 v[212:215], v[180:181], off
	v_pk_mul_f32 v[222:223], v[160:161], v[160:161]
	v_mov_b32_e32 v211, v220
	v_mov_b32_e32 v217, v221
	v_mov_b32_e32 v209, v222
	v_mov_b32_e32 v219, v223
	v_pk_add_f32 v[192:193], v[210:211], v[216:217]
	v_pk_add_f32 v[194:195], v[208:209], v[218:219]
	v_add_u32_e32 v222, s26, v162
	v_pk_add_f32 v[192:193], v[192:193], v[194:195]
	v_xor_b32_e32 v195, 4, v206
	v_add_f32_e32 v192, v192, v193
	ds_bpermute_b32 v194, v191, v192
	v_xor_b32_e32 v193, 2, v206
	v_cmp_lt_i32_e32 vcc, v193, v224
	v_mov_b32_e32 v223, 0
	s_waitcnt lgkmcnt(0)
	v_add_f32_e32 v192, v192, v194
	v_cndmask_b32_e32 v193, v206, v193, vcc
	v_lshlrev_b32_e32 v193, 2, v193
	ds_bpermute_b32 v194, v193, v192
	v_cmp_lt_i32_e32 vcc, v195, v224
	s_waitcnt lgkmcnt(0)
	v_add_f32_e32 v192, v192, v194
	v_cndmask_b32_e32 v195, v206, v195, vcc
	v_lshlrev_b32_e32 v208, 2, v195
	ds_bpermute_b32 v194, v208, v192
	v_xor_b32_e32 v195, 8, v206
	v_cmp_lt_i32_e32 vcc, v195, v224
	s_waitcnt lgkmcnt(0)
	v_add_f32_e32 v192, v192, v194
	v_cndmask_b32_e32 v195, v206, v195, vcc
	v_lshlrev_b32_e32 v209, 2, v195
	ds_bpermute_b32 v194, v209, v192
	v_xor_b32_e32 v195, 16, v206
	v_cmp_lt_i32_e32 vcc, v195, v224
	s_waitcnt lgkmcnt(0)
	v_add_f32_e32 v192, v192, v194
	v_cndmask_b32_e32 v195, v206, v195, vcc
	v_lshlrev_b32_e32 v210, 2, v195
	ds_bpermute_b32 v194, v210, v192
	v_xor_b32_e32 v195, 32, v206
	v_cmp_lt_i32_e32 vcc, v195, v224
	v_add_u32_e32 v224, s26, v200
	s_waitcnt lgkmcnt(0)
	v_add_f32_e32 v192, v192, v194
	v_cndmask_b32_e32 v195, v206, v195, vcc
	v_lshlrev_b32_e32 v195, 2, v195
	ds_bpermute_b32 v194, v195, v192
	s_waitcnt lgkmcnt(0)
	v_add_f32_e32 v192, v192, v194
	v_fmamk_f32 v192, v192, 0x3a000000, v201
	v_mul_f32_e32 v194, 0x4f800000, v192
	v_cmp_gt_f32_e32 vcc, s54, v192
	s_nop 1
	v_cndmask_b32_e32 v192, v192, v194, vcc
	v_sqrt_f32_e32 v194, v192
	s_nop 0
	v_add_u32_e32 v195, -1, v194
	v_add_u32_e32 v211, 1, v194
	v_fma_f32 v216, -v195, v194, v192
	v_fma_f32 v217, -v211, v194, v192
	v_cmp_ge_f32_e64 s[16:17], 0, v216
	s_nop 1
	v_cndmask_b32_e64 v194, v194, v195, s[16:17]
	v_cmp_lt_f32_e64 s[16:17], 0, v217
	s_nop 1
	v_cndmask_b32_e64 v194, v194, v211, s[16:17]
	v_mul_f32_e32 v195, 0x37800000, v194
	v_cndmask_b32_e32 v194, v194, v195, vcc
	v_cmp_class_f32_e32 vcc, v192, v202
	v_mov_b32_e32 v211, 0
	s_nop 0
	v_cndmask_b32_e32 v192, v194, v192, vcc
	v_div_scale_f32 v194, s[16:17], v192, v192, 1.0
	v_rcp_f32_e32 v195, v194
	v_div_scale_f32 v216, vcc, 1.0, v192, 1.0
	s_lshl_b64 s[16:17], s[52:53], 11
	v_fma_f32 v217, -v194, v195, 1.0
	v_fmac_f32_e32 v195, v217, v195
	v_mul_f32_e32 v217, v216, v195
	v_fma_f32 v218, -v194, v217, v216
	v_fmac_f32_e32 v217, v218, v195
	v_fma_f32 v194, -v194, v217, v216
	v_div_fmas_f32 v194, v194, v195, v217
	v_div_fixup_f32 v192, v194, v192, 1.0
	v_pk_mul_f32 v[194:195], v[192:193], v[130:131] op_sel_hi:[0,1]
	s_waitcnt vmcnt(0)
	v_pk_mul_f32 v[212:213], v[194:195], v[212:213]
	v_pk_mul_f32 v[194:195], v[192:193], v[132:133] op_sel_hi:[0,1]
	v_cvt_pk_fp8_f32 v211, v212, v213
	v_pk_mul_f32 v[214:215], v[194:195], v[214:215]
	v_lshl_add_u64 v[194:195], v[172:173], 0, s[16:17]
	s_cmpk_gt_i32 s55, 0x7ff
	v_cvt_pk_fp8_f32 v211, v214, v215 op_sel:[0,0,1]
	s_cselect_b64 s[16:17], -1, 0
	s_and_b64 vcc, exec, s[16:17]
	global_store_dword v[194:195], v211, off
	v_cvt_pk_bf16_f32 v216, v212, v213
	v_cvt_pk_bf16_f32 v217, v214, v215
	s_nop 0
	v_lshlrev_b32_e32 v211, 16, v216
	v_and_b32_e32 v218, 0xffff0000, v216
	v_lshlrev_b32_e32 v219, 16, v217
	v_and_b32_e32 v220, 0xffff0000, v217
	v_sub_f32_e32 v211, v212, v211
	v_sub_f32_e32 v212, v213, v218
	v_sub_f32_e32 v213, v214, v219
	v_sub_f32_e32 v214, v215, v220
	v_cvt_pk_bf16_f32 v218, v211, v212
	v_cvt_pk_bf16_f32 v219, v213, v214
	global_load_dwordx4 v[212:215], v[180:181], off offset:1024
	v_pk_mul_f32 v[220:221], v[192:193], v[134:135] op_sel_hi:[0,1]
	v_mov_b32_e32 v211, 0
	s_waitcnt vmcnt(0)
	v_pk_mul_f32 v[212:213], v[220:221], v[212:213]
	s_nop 0
	v_cvt_pk_fp8_f32 v211, v212, v213
	v_pk_mul_f32 v[220:221], v[192:193], v[136:137] op_sel_hi:[0,1]
	v_pk_mul_f32 v[214:215], v[220:221], v[214:215]
	v_add_u32_e32 v220, s27, v162
	v_cvt_pk_fp8_f32 v211, v214, v215 op_sel:[0,0,1]
	ds_write_b64 v222, v[216:217]
	ds_write_b64 v220, v[218:219]
	v_add_u32_e32 v222, s26, v167
	global_store_dword v[194:195], v211, off offset:256
	v_cvt_pk_bf16_f32 v216, v212, v213
	v_cvt_pk_bf16_f32 v217, v214, v215
	s_nop 0
	v_lshlrev_b32_e32 v211, 16, v216
	v_and_b32_e32 v218, 0xffff0000, v216
	v_lshlrev_b32_e32 v219, 16, v217
	v_and_b32_e32 v220, 0xffff0000, v217
	v_sub_f32_e32 v211, v212, v211
	v_sub_f32_e32 v212, v213, v218
	v_sub_f32_e32 v213, v214, v219
	v_sub_f32_e32 v214, v215, v220
	v_cvt_pk_bf16_f32 v218, v211, v212
	v_cvt_pk_bf16_f32 v219, v213, v214
	global_load_dwordx4 v[212:215], v[180:181], off offset:2048
	v_pk_mul_f32 v[220:221], v[192:193], v[138:139] op_sel_hi:[0,1]
	v_mov_b32_e32 v211, 0
	s_waitcnt vmcnt(0)
; #define LAS __attribute__((address_space(3)))
; __device__ __forceinline__ unsigned cvtpk(float lo, float hi) { unsigned r; asm volatile("v_cvt_pk_bf16_f32 %0, %1, %2" : "=v"(r) : "v"(lo), "v"(hi)); return r; }
; __device__ __forceinline__ unsigned cvt4_fp8(float a, float b, float c, float d) { int w = 0; w = __builtin_amdgcn_cvt_pk_fp8_f32(a, b, w, false); w = __builtin_amdgcn_cvt_pk_fp8_f32(c, d, w, true); return (unsigned)w; }
; __device__ __forceinline__ float bflo(unsigned w) { return __uint_as_float(w << 16); }
; __device__ __forceinline__ float bfhi(unsigned w) { return __uint_as_float(w & 0xffff0000u); }
; __global__ void __launch_bounds__(512, 2) mega_fwd(Args args) {
;     ...
;                 for (int j = 0; j < 8; ++j) { const f32x4 gv = ((const f32x4*)gn)[64 * j + lane]; const f32x4 y = nv[r][j] * rstd * gv;
;                     o4[64 * j] = cvt4_fp8(y[0], y[1], y[2], y[3]);
;                     u32x2 hw, lw; hw.x = cvtpk(y[0], y[1]); hw.y = cvtpk(y[2], y[3]);
;                     lw.x = cvtpk(y[0] - bflo(hw.x), y[1] - bfhi(hw.x)); lw.y = cvtpk(y[2] - bflo(hw.y), y[3] - bfhi(hw.y));
;                     *(LAS u32x2*)(Ahi + rowc * AST + (64 * j + lane) * 8) = hw; *(LAS u32x2*)(Alo + rowc * AST + (64 * j + lane) * 8) = lw; } }
;             if (ch + G < T / CR) {
; #pragma unroll
;                 for (int r = 0; r < RPW; ++r) { const f32x4* xr = (const f32x4*)(x + (size_t)((ch + G) * CR + wave * RPW + r) * DM) + lane;
; #pragma unroll
;                     for (int j = 0; j < 8; ++j) nv[r][j] = xr[64 * j]; } }
	v_pk_mul_f32 v[212:213], v[220:221], v[212:213]
	s_nop 0
	v_cvt_pk_fp8_f32 v211, v212, v213
	v_pk_mul_f32 v[220:221], v[192:193], v[140:141] op_sel_hi:[0,1]
	v_pk_mul_f32 v[214:215], v[220:221], v[214:215]
	v_add_u32_e32 v220, s27, v167
	v_cvt_pk_fp8_f32 v211, v214, v215 op_sel:[0,0,1]
	ds_write_b64 v222, v[216:217]
	ds_write_b64 v220, v[218:219]
	v_add_u32_e32 v222, s26, v179
	global_store_dword v[194:195], v211, off offset:512
	v_cvt_pk_bf16_f32 v216, v212, v213
	v_cvt_pk_bf16_f32 v217, v214, v215
	s_nop 0
	v_lshlrev_b32_e32 v211, 16, v216
	v_and_b32_e32 v218, 0xffff0000, v216
	v_lshlrev_b32_e32 v219, 16, v217
	v_and_b32_e32 v220, 0xffff0000, v217
	v_sub_f32_e32 v211, v212, v211
	v_sub_f32_e32 v212, v213, v218
	v_sub_f32_e32 v213, v214, v219
	v_sub_f32_e32 v214, v215, v220
	v_cvt_pk_bf16_f32 v218, v211, v212
	v_cvt_pk_bf16_f32 v219, v213, v214
	global_load_dwordx4 v[212:215], v[180:181], off offset:3072
	v_pk_mul_f32 v[220:221], v[192:193], v[142:143] op_sel_hi:[0,1]
	v_mov_b32_e32 v211, 0
	s_waitcnt vmcnt(0)
	v_pk_mul_f32 v[212:213], v[220:221], v[212:213]
	s_nop 0
	v_cvt_pk_fp8_f32 v211, v212, v213
	v_pk_mul_f32 v[220:221], v[192:193], v[144:145] op_sel_hi:[0,1]
	v_pk_mul_f32 v[214:215], v[220:221], v[214:215]
	v_add_u32_e32 v220, s27, v179
	v_cvt_pk_fp8_f32 v211, v214, v215 op_sel:[0,0,1]
	ds_write_b64 v222, v[216:217]
	ds_write_b64 v220, v[218:219]
	v_add_u32_e32 v222, s26, v196
	global_store_dword v[194:195], v211, off offset:768
	v_cvt_pk_bf16_f32 v216, v212, v213
	v_cvt_pk_bf16_f32 v217, v214, v215
	s_nop 0
	v_lshlrev_b32_e32 v211, 16, v216
	v_and_b32_e32 v218, 0xffff0000, v216
	v_lshlrev_b32_e32 v219, 16, v217
	v_and_b32_e32 v220, 0xffff0000, v217
	v_sub_f32_e32 v211, v212, v211
	v_sub_f32_e32 v212, v213, v218
	v_sub_f32_e32 v213, v214, v219
	v_sub_f32_e32 v214, v215, v220
	v_cvt_pk_bf16_f32 v218, v211, v212
	v_cvt_pk_bf16_f32 v219, v213, v214
	global_load_dwordx4 v[212:215], v[182:183], off
	v_pk_mul_f32 v[220:221], v[192:193], v[146:147] op_sel_hi:[0,1]
	v_mov_b32_e32 v211, 0
	s_waitcnt vmcnt(0)
	v_pk_mul_f32 v[212:213], v[220:221], v[212:213]
	s_nop 0
	v_cvt_pk_fp8_f32 v211, v212, v213
	v_pk_mul_f32 v[220:221], v[192:193], v[148:149] op_sel_hi:[0,1]
	v_pk_mul_f32 v[214:215], v[220:221], v[214:215]
	v_add_u32_e32 v220, s27, v196
	v_cvt_pk_fp8_f32 v211, v214, v215 op_sel:[0,0,1]
	ds_write_b64 v222, v[216:217]
	ds_write_b64 v220, v[218:219]
	v_add_u32_e32 v222, s26, v197
	global_store_dword v[194:195], v211, off offset:1024
	v_cvt_pk_bf16_f32 v216, v212, v213
	v_cvt_pk_bf16_f32 v217, v214, v215
	s_nop 0
	v_lshlrev_b32_e32 v211, 16, v216
	v_and_b32_e32 v218, 0xffff0000, v216
	v_lshlrev_b32_e32 v219, 16, v217
	v_and_b32_e32 v220, 0xffff0000, v217
	v_sub_f32_e32 v211, v212, v211
	v_sub_f32_e32 v212, v213, v218
	v_sub_f32_e32 v213, v214, v219
	v_sub_f32_e32 v214, v215, v220
	v_cvt_pk_bf16_f32 v218, v211, v212
	v_cvt_pk_bf16_f32 v219, v213, v214
	global_load_dwordx4 v[212:215], v[184:185], off
	v_pk_mul_f32 v[220:221], v[192:193], v[150:151] op_sel_hi:[0,1]
	v_mov_b32_e32 v211, 0
	s_waitcnt vmcnt(0)
	v_pk_mul_f32 v[212:213], v[220:221], v[212:213]
	s_nop 0
	v_cvt_pk_fp8_f32 v211, v212, v213
	v_pk_mul_f32 v[220:221], v[192:193], v[152:153] op_sel_hi:[0,1]
	v_pk_mul_f32 v[214:215], v[220:221], v[214:215]
	v_add_u32_e32 v220, s27, v197
	v_cvt_pk_fp8_f32 v211, v214, v215 op_sel:[0,0,1]
	ds_write_b64 v222, v[216:217]
	ds_write_b64 v220, v[218:219]
	v_add_u32_e32 v222, s26, v198
	global_store_dword v[194:195], v211, off offset:1280
	v_cvt_pk_bf16_f32 v216, v212, v213
	v_cvt_pk_bf16_f32 v217, v214, v215
	s_nop 0
	v_lshlrev_b32_e32 v211, 16, v216
	v_and_b32_e32 v218, 0xffff0000, v216
	v_lshlrev_b32_e32 v219, 16, v217
	v_and_b32_e32 v220, 0xffff0000, v217
	v_sub_f32_e32 v211, v212, v211
	v_sub_f32_e32 v212, v213, v218
	v_sub_f32_e32 v213, v214, v219
	v_sub_f32_e32 v214, v215, v220
	v_cvt_pk_bf16_f32 v218, v211, v212
	v_cvt_pk_bf16_f32 v219, v213, v214
	global_load_dwordx4 v[212:215], v[186:187], off
	v_pk_mul_f32 v[220:221], v[192:193], v[154:155] op_sel_hi:[0,1]
	v_mov_b32_e32 v211, 0
	s_waitcnt vmcnt(0)
	v_pk_mul_f32 v[212:213], v[220:221], v[212:213]
	s_nop 0
	v_cvt_pk_fp8_f32 v211, v212, v213
	v_pk_mul_f32 v[220:221], v[192:193], v[156:157] op_sel_hi:[0,1]
	v_pk_mul_f32 v[214:215], v[220:221], v[214:215]
	v_add_u32_e32 v220, s27, v198
	v_cvt_pk_fp8_f32 v211, v214, v215 op_sel:[0,0,1]
	ds_write_b64 v222, v[216:217]
	ds_write_b64 v220, v[218:219]
	v_add_u32_e32 v222, s27, v199
	global_store_dword v[194:195], v211, off offset:1536
	v_cvt_pk_bf16_f32 v216, v212, v213
	v_cvt_pk_bf16_f32 v217, v214, v215
	s_nop 0
	v_lshlrev_b32_e32 v211, 16, v216
	v_and_b32_e32 v218, 0xffff0000, v216
	v_lshlrev_b32_e32 v219, 16, v217
	v_and_b32_e32 v220, 0xffff0000, v217
	v_sub_f32_e32 v211, v212, v211
	v_sub_f32_e32 v212, v213, v218
	v_sub_f32_e32 v213, v214, v219
	v_sub_f32_e32 v214, v215, v220
	v_cvt_pk_bf16_f32 v218, v211, v212
	v_cvt_pk_bf16_f32 v219, v213, v214
	global_load_dwordx4 v[212:215], v[188:189], off
	v_pk_mul_f32 v[220:221], v[192:193], v[158:159] op_sel_hi:[0,1]
	v_add_u32_e32 v211, s26, v199
	ds_write_b64 v211, v[216:217]
	ds_write_b64 v222, v[218:219]
	s_waitcnt vmcnt(0)
	v_pk_mul_f32 v[212:213], v[220:221], v[212:213]
	s_nop 0
	v_cvt_pk_fp8_f32 v223, v212, v213
	v_pk_mul_f32 v[220:221], v[192:193], v[160:161] op_sel_hi:[0,1]
	v_pk_mul_f32 v[214:215], v[220:221], v[214:215]
	s_nop 0
	v_cvt_pk_fp8_f32 v223, v214, v215 op_sel:[0,0,1]
	global_store_dword v[194:195], v223, off offset:1792
	v_cvt_pk_bf16_f32 v194, v212, v213
	v_cvt_pk_bf16_f32 v195, v214, v215
	s_nop 0
	v_and_b32_e32 v211, 0xffff0000, v194
	v_lshlrev_b32_e32 v216, 16, v195
	v_lshlrev_b32_e32 v192, 16, v194
	v_and_b32_e32 v217, 0xffff0000, v195
	v_sub_f32_e32 v211, v213, v211
	v_sub_f32_e32 v213, v214, v216
	v_sub_f32_e32 v192, v212, v192
	v_sub_f32_e32 v214, v215, v217
	v_cvt_pk_bf16_f32 v212, v192, v211
	v_cvt_pk_bf16_f32 v213, v213, v214
	ds_write_b64 v224, v[194:195]
	ds_write_b64 v225, v[212:213]
	s_cbranch_vccnz .LBB0_1998
	s_add_i32 s52, s41, s3
	s_ashr_i32 s53, s52, 31
	s_lshl_b64 s[52:53], s[52:53], 13
	v_lshl_add_u64 v[146:147], v[174:175], 0, s[52:53]
	v_add_co_u32_e32 v158, vcc, 0x1000, v146
	global_load_dwordx4 v[130:133], v[146:147], off
	global_load_dwordx4 v[134:137], v[146:147], off offset:1024
	global_load_dwordx4 v[138:141], v[146:147], off offset:2048
	global_load_dwordx4 v[142:145], v[146:147], off offset:3072
	v_addc_co_u32_e32 v159, vcc, 0, v147, vcc
	global_load_dwordx4 v[146:149], v[158:159], off
	global_load_dwordx4 v[150:153], v[158:159], off offset:1024
	global_load_dwordx4 v[154:157], v[158:159], off offset:2048
	s_nop 0
	global_load_dwordx4 v[158:161], v[158:159], off offset:3072

; __device__ __forceinline__ float bflo(unsigned w) { return __uint_as_float(w << 16); }
; __device__ __forceinline__ float bfhi(unsigned w) { return __uint_as_float(w & 0xffff0000u); }
; __global__ void __launch_bounds__(512, 2) mega_fwd(Args args) {
;     ...
;         const float* gn = args.in[I_PLE_NORM]; int ln = lane; asm volatile("" : "+v"(ln));
;         for (int m = gw - NP13 * 8; m < T; m += NGW - NP13 * 8) { u32x2* hr = (u32x2*)(H1 + (size_t)m * DM) + ln; f32x4 v[8];
; #pragma unroll
;             for (int j = 0; j < 8; ++j) { const u32x2 h_ = hr[64 * j]; v[j] = (f32x4){bflo(h_.x), bfhi(h_.x), bflo(h_.y), bfhi(h_.y)}; }
; #pragma unroll
;             for (int k = 0; k < 4; ++k) { const int dest = tab[AE[m * 4 + k]] + AP[m * 4 + k]; const float w = AW[m * 4 + k] * 0.125f; const int* yr = (const int*)(YY + (size_t)dest * DM) + ln;
; #pragma unroll
;                 for (int j = 0; j < 8; ++j) { const int y = yr[64 * j]; const f32x2 ylo = __builtin_amdgcn_cvt_pk_f32_fp8(y, false), yhi = __builtin_amdgcn_cvt_pk_f32_fp8(y, true);
;                     v[j][0] += w * ylo.x; v[j][1] += w * ylo.y; v[j][2] += w * yhi.x; v[j][3] += w * yhi.y; } }
.LBB0_2654:
	s_lshl_b32 s4, s3, 3
	s_sub_i32 s6, s38, s4
	s_waitcnt vmcnt(12)
	v_mov_b32_e32 v14, v164
	s_cmpk_gt_i32 s6, 0x3fff
	s_cbranch_scc1 .LBB0_2657
	s_load_dwordx2 s[12:13], s[0:1], 0xa8
	v_ashrrev_i32_e32 v15, 31, v14
	s_sub_i32 s10, s40, s4
	s_mov_b64 s[4:5], 0x1000
	s_ashr_i32 s7, s6, 31
	s_waitcnt lgkmcnt(0)
	v_lshl_add_u64 v[4:5], v[14:15], 4, s[12:13]
	v_lshl_add_u64 v[6:7], v[4:5], 0, s[4:5]
	s_mov_b64 s[4:5], 0x1400
	v_lshl_add_u64 v[8:9], v[4:5], 0, s[4:5]
	s_mov_b64 s[4:5], 0x1800
	v_lshl_add_u64 v[10:11], v[4:5], 0, s[4:5]
	s_mov_b64 s[4:5], 0x1c00
	v_lshl_add_u64 v[12:13], v[4:5], 0, s[4:5]
	s_lshl_b64 s[4:5], s[6:7], 12
	s_waitcnt vmcnt(2)
	v_mbcnt_lo_u32_b32 v18, -1, 0
	v_lshlrev_b64 v[16:17], 2, v[14:15]
	v_lshl_add_u64 v[14:15], v[14:15], 3, s[4:5]
	s_lshl_b64 s[4:5], s[6:7], 11
	v_mbcnt_hi_u32_b32 v22, -1, v18
	v_lshl_add_u64 v[2:3], s[28:29], 0, v[16:17]
	s_ashr_i32 s11, s10, 31
	v_lshl_add_u64 v[16:17], s[4:5], 0, v[16:17]
	s_lshl_b32 s4, s82, 5
	s_lshl_b32 s3, s3, 5
	v_and_b32_e32 v18, 64, v22
	s_lshl_b64 s[12:13], s[10:11], 12
	s_lshl_b64 s[16:17], s[10:11], 11
	s_lshl_b32 s28, s6, 2
	s_sub_i32 s3, s4, s3
	v_mov_b32_e32 v1, 0
	s_add_i32 s7, 0, 0x25800
	s_mov_b32 s30, 0x3e000000
	v_add_u32_e32 v23, 64, v18
	v_xor_b32_e32 v24, 1, v22
	v_xor_b32_e32 v25, 2, v22
	s_waitcnt vmcnt(0)
	v_xor_b32_e32 v26, 4, v22
	v_xor_b32_e32 v27, 8, v22
	v_xor_b32_e32 v28, 16, v22
	v_xor_b32_e32 v29, 32, v22
	v_mov_b32_e32 v30, 0x358637bd
	s_mov_b32 s11, 0xf800000
	v_mov_b32_e32 v31, 0x260
	s_mov_b32 s26, 0x25000000
	global_load_dwordx4 v[212:215], v[4:5], off offset:1024
	global_load_dwordx4 v[216:219], v[4:5], off offset:2048
	global_load_dwordx4 v[220:223], v[4:5], off offset:3072
	global_load_dwordx4 v[224:227], v[6:7], off
	global_load_dwordx4 v[228:231], v[8:9], off
	global_load_dwordx4 v[232:235], v[10:11], off
	global_load_dwordx4 v[236:239], v[12:13], off
	s_waitcnt vmcnt(0)
.LBB0_2656:
	v_cmp_lt_i32_e32 vcc, v24, v23
	v_lshl_add_u64 v[20:21], s[18:19], 0, v[16:17]
	s_ashr_i32 s29, s28, 31
	v_cndmask_b32_e32 v33, v22, v24, vcc
	v_cmp_lt_i32_e32 vcc, v25, v23
	v_add_co_u32_e64 v20, s[4:5], s26, v20
	s_nop 0
	v_cndmask_b32_e32 v34, v22, v25, vcc
	v_cmp_lt_i32_e32 vcc, v26, v23
	v_lshl_add_u64 v[18:19], s[18:19], 0, v[14:15]
	s_lshl_b64 s[22:23], s[28:29], 2
	v_cndmask_b32_e32 v35, v22, v26, vcc
	v_cmp_lt_i32_e32 vcc, v27, v23
	v_addc_co_u32_e64 v21, s[4:5], 0, v21, s[4:5]
	s_nop 0
	v_cndmask_b32_e32 v39, v22, v27, vcc
	v_cmp_lt_i32_e32 vcc, v28, v23
	s_add_u32 s4, s42, s22
	s_addc_u32 s5, s43, s23
	v_cndmask_b32_e32 v40, v22, v28, vcc
	v_cmp_lt_i32_e32 vcc, v29, v23
	v_lshlrev_b32_e32 v38, 2, v33
	v_lshlrev_b32_e32 v37, 2, v34
	v_cndmask_b32_e32 v41, v22, v29, vcc
	v_add_co_u32_e32 v18, vcc, 0x1d000000, v18
	v_lshlrev_b32_e32 v34, 2, v40
	s_nop 0
	v_addc_co_u32_e32 v19, vcc, 0, v19, vcc
	v_lshlrev_b32_e32 v33, 2, v41
	global_load_dwordx2 v[48:49], v[18:19], off
	global_load_dwordx2 v[50:51], v[18:19], off offset:512
	global_load_dwordx2 v[52:53], v[18:19], off offset:1024
	global_load_dwordx2 v[54:55], v[18:19], off offset:1536
	global_load_dwordx2 v[56:57], v[18:19], off offset:2048
	global_load_dwordx2 v[58:59], v[18:19], off offset:2560
	global_load_dwordx2 v[60:61], v[18:19], off offset:3072
	global_load_dwordx2 v[62:63], v[18:19], off offset:3584
	global_load_dwordx4 v[40:43], v1, s[4:5]
	s_add_u32 s4, s44, s22
	s_addc_u32 s5, s45, s23
	v_lshlrev_b32_e32 v36, 2, v35
	v_lshlrev_b32_e32 v35, 2, v39
	global_load_dword v39, v1, s[4:5]
	s_add_u32 s4, s46, s22
	s_addc_u32 s5, s47, s23
	s_add_i32 s22, s28, 1
	s_ashr_i32 s23, s22, 31
	global_load_dword v64, v1, s[4:5]
	s_lshl_b64 s[4:5], s[22:23], 2
	s_add_u32 s22, s44, s4
	s_addc_u32 s23, s45, s5
	global_load_dwordx3 v[44:46], v1, s[22:23]
	s_add_u32 s4, s46, s4
	s_addc_u32 s5, s47, s5
	global_load_dword v65, v1, s[4:5]
	s_add_i32 s22, s28, 2
	s_ashr_i32 s23, s22, 31
	s_lshl_b64 s[4:5], s[22:23], 2
	s_add_u32 s4, s46, s4
	s_addc_u32 s5, s47, s5
	v_mov_b32_e32 v32, 0
	s_add_i32 s6, s6, s10
	s_add_i32 s28, s28, s3
	v_lshl_add_u64 v[14:15], v[14:15], 0, s[12:13]
	v_lshl_add_u64 v[16:17], v[16:17], 0, s[16:17]
	s_cmpk_lt_i32 s6, 0x4000
	s_waitcnt vmcnt(12)
	v_lshlrev_b32_e32 v165, 16, v48
	s_waitcnt vmcnt(11)
	v_lshlrev_b32_e32 v182, 16, v50
	v_and_b32_e32 v183, 0xffff0000, v50
	v_lshlrev_b32_e32 v184, 16, v51
	v_and_b32_e32 v185, 0xffff0000, v51
	s_waitcnt vmcnt(10)
	v_lshlrev_b32_e32 v186, 16, v52
	v_and_b32_e32 v187, 0xffff0000, v52
	s_waitcnt vmcnt(9)
	v_lshlrev_b32_e32 v190, 16, v54
	s_waitcnt vmcnt(4)
	v_lshlrev_b32_e32 v40, 2, v40
	v_lshlrev_b32_e32 v41, 2, v41
	v_lshlrev_b32_e32 v42, 2, v42
	v_lshlrev_b32_e32 v43, 2, v43
	v_add_u32_e32 v40, s7, v40
	v_add_u32_e32 v41, s7, v41
	v_add_u32_e32 v42, s7, v42
	v_add_u32_e32 v43, s7, v43
	ds_read_b32 v40, v40
	ds_read_b32 v47, v41
	ds_read_b32 v50, v42
	ds_read_b32 v51, v43
	v_and_b32_e32 v191, 0xffff0000, v54
	s_waitcnt vmcnt(3) lgkmcnt(3)
	v_add_u32_e32 v40, v39, v40
	v_ashrrev_i32_e32 v41, 31, v40
	v_lshlrev_b64 v[40:41], 11, v[40:41]
	v_lshl_add_u64 v[40:41], v[2:3], 0, v[40:41]
	v_lshlrev_b32_e32 v198, 16, v58
	v_and_b32_e32 v199, 0xffff0000, v58
	v_lshlrev_b32_e32 v206, 16, v62
	v_and_b32_e32 v207, 0xffff0000, v62
	global_load_dword v39, v[40:41], off
	global_load_dword v52, v[40:41], off offset:256
	global_load_dword v54, v[40:41], off offset:512
	global_load_dword v58, v[40:41], off offset:768
	global_load_dword v62, v[40:41], off offset:1024
	global_load_dword v66, v[40:41], off offset:1280
	global_load_dword v70, v[40:41], off offset:1536
	global_load_dword v74, v[40:41], off offset:1792
	global_load_dwordx2 v[42:43], v1, s[4:5]
	s_waitcnt vmcnt(10) lgkmcnt(2)
; __device__ __forceinline__ float bflo(unsigned w) { return __uint_as_float(w << 16); }
; __device__ __forceinline__ float bfhi(unsigned w) { return __uint_as_float(w & 0xffff0000u); }
; __global__ void __launch_bounds__(512, 2) mega_fwd(Args args) {
;     ...
;             for (int j = 0; j < 8; ++j) { const u32x2 h_ = hr[64 * j]; v[j] = (f32x4){bflo(h_.x), bfhi(h_.x), bflo(h_.y), bfhi(h_.y)}; }
; #pragma unroll
;             for (int k = 0; k < 4; ++k) { const int dest = tab[AE[m * 4 + k]] + AP[m * 4 + k]; const float w = AW[m * 4 + k] * 0.125f; const int* yr = (const int*)(YY + (size_t)dest * DM) + ln;
; #pragma unroll
;                 for (int j = 0; j < 8; ++j) { const int y = yr[64 * j]; const f32x2 ylo = __builtin_amdgcn_cvt_pk_f32_fp8(y, false), yhi = __builtin_amdgcn_cvt_pk_f32_fp8(y, true);
;                     v[j][0] += w * ylo.x; v[j][1] += w * ylo.y; v[j][2] += w * yhi.x; v[j][3] += w * yhi.y; } }
	v_add_u32_e32 v40, v44, v47
	s_waitcnt lgkmcnt(1)
	v_add_u32_e32 v44, v45, v50
	s_waitcnt lgkmcnt(0)
	v_add_u32_e32 v46, v46, v51
	v_ashrrev_i32_e32 v41, 31, v40
	v_ashrrev_i32_e32 v45, 31, v44
	v_ashrrev_i32_e32 v47, 31, v46
	v_lshlrev_b64 v[40:41], 11, v[40:41]
	v_lshlrev_b64 v[44:45], 11, v[44:45]
	v_lshlrev_b64 v[46:47], 11, v[46:47]
	v_lshl_add_u64 v[40:41], v[2:3], 0, v[40:41]
	v_lshl_add_u64 v[44:45], v[2:3], 0, v[44:45]
	v_lshl_add_u64 v[46:47], v[2:3], 0, v[46:47]
	global_load_dword v78, v[40:41], off
	global_load_dword v81, v[40:41], off offset:256
	global_load_dword v83, v[40:41], off offset:512
	global_load_dword v94, v[40:41], off offset:768
	global_load_dword v98, v[40:41], off offset:1024
	global_load_dword v102, v[40:41], off offset:1280
	global_load_dword v106, v[40:41], off offset:1536
	global_load_dword v110, v[40:41], off offset:1792
	global_load_dword v114, v[44:45], off
	global_load_dword v118, v[44:45], off offset:256
	global_load_dword v122, v[44:45], off offset:512
	global_load_dword v126, v[44:45], off offset:768
	global_load_dword v130, v[44:45], off offset:1024
	global_load_dword v134, v[44:45], off offset:1280
	global_load_dword v138, v[44:45], off offset:1536
	global_load_dword v142, v[44:45], off offset:1792
	global_load_dword v146, v[46:47], off
	global_load_dword v150, v[46:47], off offset:256
	global_load_dword v154, v[46:47], off offset:512
	global_load_dword v158, v[46:47], off offset:768
	global_load_dword v162, v[46:47], off offset:1024
	global_load_dword v170, v[46:47], off offset:1280
	global_load_dword v174, v[46:47], off offset:1536
	global_load_dword v178, v[46:47], off offset:1792
	v_and_b32_e32 v167, 0xffff0000, v48
	v_lshlrev_b32_e32 v180, 16, v49
	v_and_b32_e32 v181, 0xffff0000, v49
	v_lshlrev_b32_e32 v188, 16, v53
	v_and_b32_e32 v189, 0xffff0000, v53
	v_lshlrev_b32_e32 v192, 16, v55
	v_and_b32_e32 v193, 0xffff0000, v55
	v_lshlrev_b32_e32 v194, 16, v56
	v_and_b32_e32 v195, 0xffff0000, v56
	v_lshlrev_b32_e32 v196, 16, v57
	v_and_b32_e32 v197, 0xffff0000, v57
	v_lshlrev_b32_e32 v200, 16, v59
	v_and_b32_e32 v201, 0xffff0000, v59
	v_lshlrev_b32_e32 v202, 16, v60
	v_and_b32_e32 v203, 0xffff0000, v60
	v_lshlrev_b32_e32 v204, 16, v61
	v_and_b32_e32 v205, 0xffff0000, v61
	v_lshlrev_b32_e32 v208, 16, v63
	v_and_b32_e32 v209, 0xffff0000, v63
	s_waitcnt vmcnt(33)
	v_pk_mul_f32 v[48:49], v[64:65], s[30:31] op_sel_hi:[1,0]
	s_waitcnt vmcnt(23)
	v_cvt_pk_f32_fp8_e32 v[76:77], v78
	v_cvt_pk_f32_fp8_sdwa v[78:79], v78 src0_sel:WORD_1
	s_waitcnt vmcnt(22)
	v_cvt_pk_f32_fp8_e32 v[84:85], v81
	v_cvt_pk_f32_fp8_e32 v[40:41], v39
	v_cvt_pk_f32_fp8_sdwa v[44:45], v39 src0_sel:WORD_1
	v_cvt_pk_f32_fp8_e32 v[46:47], v52
	v_cvt_pk_f32_fp8_sdwa v[50:51], v52 src0_sel:WORD_1
	v_cvt_pk_f32_fp8_sdwa v[86:87], v81 src0_sel:WORD_1
	v_cvt_pk_f32_fp8_e32 v[52:53], v54
	v_cvt_pk_f32_fp8_sdwa v[54:55], v54 src0_sel:WORD_1
	v_cvt_pk_f32_fp8_e32 v[56:57], v58
	v_cvt_pk_f32_fp8_sdwa v[58:59], v58 src0_sel:WORD_1
	v_cvt_pk_f32_fp8_e32 v[60:61], v62
	v_cvt_pk_f32_fp8_sdwa v[62:63], v62 src0_sel:WORD_1
	v_cvt_pk_f32_fp8_e32 v[64:65], v66
	v_cvt_pk_f32_fp8_sdwa v[66:67], v66 src0_sel:WORD_1
	v_cvt_pk_f32_fp8_e32 v[68:69], v70
	v_cvt_pk_f32_fp8_sdwa v[70:71], v70 src0_sel:WORD_1
	v_cvt_pk_f32_fp8_e32 v[72:73], v74
	v_cvt_pk_f32_fp8_sdwa v[74:75], v74 src0_sel:WORD_1
	s_waitcnt vmcnt(21)
	v_cvt_pk_f32_fp8_e32 v[88:89], v83
	v_cvt_pk_f32_fp8_sdwa v[90:91], v83 src0_sel:WORD_1
	s_waitcnt vmcnt(20)
	v_cvt_pk_f32_fp8_e32 v[92:93], v94
	v_cvt_pk_f32_fp8_sdwa v[94:95], v94 src0_sel:WORD_1
	s_waitcnt vmcnt(19)
	v_cvt_pk_f32_fp8_e32 v[96:97], v98
	v_cvt_pk_f32_fp8_sdwa v[98:99], v98 src0_sel:WORD_1
	s_waitcnt vmcnt(18)
	v_cvt_pk_f32_fp8_e32 v[100:101], v102
	v_cvt_pk_f32_fp8_sdwa v[102:103], v102 src0_sel:WORD_1
	s_waitcnt vmcnt(17)
	v_cvt_pk_f32_fp8_e32 v[104:105], v106
	v_cvt_pk_f32_fp8_sdwa v[106:107], v106 src0_sel:WORD_1
	s_waitcnt vmcnt(16)
	v_cvt_pk_f32_fp8_e32 v[108:109], v110
	v_cvt_pk_f32_fp8_sdwa v[110:111], v110 src0_sel:WORD_1
	s_waitcnt vmcnt(15)
	v_cvt_pk_f32_fp8_e32 v[112:113], v114
	v_cvt_pk_f32_fp8_sdwa v[114:115], v114 src0_sel:WORD_1
	s_waitcnt vmcnt(14)
	v_cvt_pk_f32_fp8_e32 v[116:117], v118
	v_cvt_pk_f32_fp8_sdwa v[118:119], v118 src0_sel:WORD_1
	s_waitcnt vmcnt(7)
	v_cvt_pk_f32_fp8_e32 v[144:145], v146
	v_cvt_pk_f32_fp8_sdwa v[146:147], v146 src0_sel:WORD_1
	s_waitcnt vmcnt(6)
	v_cvt_pk_f32_fp8_e32 v[148:149], v150
	v_cvt_pk_f32_fp8_sdwa v[150:151], v150 src0_sel:WORD_1
	v_cvt_pk_f32_fp8_e32 v[120:121], v122
	v_cvt_pk_f32_fp8_sdwa v[122:123], v122 src0_sel:WORD_1
	v_cvt_pk_f32_fp8_e32 v[124:125], v126
	v_cvt_pk_f32_fp8_sdwa v[126:127], v126 src0_sel:WORD_1
	v_cvt_pk_f32_fp8_e32 v[128:129], v130
	v_cvt_pk_f32_fp8_sdwa v[130:131], v130 src0_sel:WORD_1
	v_cvt_pk_f32_fp8_e32 v[132:133], v134
	v_cvt_pk_f32_fp8_sdwa v[134:135], v134 src0_sel:WORD_1
	v_cvt_pk_f32_fp8_e32 v[136:137], v138
	v_cvt_pk_f32_fp8_sdwa v[138:139], v138 src0_sel:WORD_1
	v_cvt_pk_f32_fp8_e32 v[140:141], v142
	v_cvt_pk_f32_fp8_sdwa v[142:143], v142 src0_sel:WORD_1
	s_waitcnt vmcnt(5)
	v_cvt_pk_f32_fp8_e32 v[152:153], v154
	v_cvt_pk_f32_fp8_sdwa v[154:155], v154 src0_sel:WORD_1
	s_waitcnt vmcnt(4)
	v_cvt_pk_f32_fp8_e32 v[156:157], v158
	v_cvt_pk_f32_fp8_sdwa v[158:159], v158 src0_sel:WORD_1
	s_waitcnt vmcnt(3)
	v_cvt_pk_f32_fp8_e32 v[160:161], v162
	v_cvt_pk_f32_fp8_sdwa v[162:163], v162 src0_sel:WORD_1
	s_waitcnt vmcnt(2)
	v_cvt_pk_f32_fp8_e32 v[168:169], v170
	v_cvt_pk_f32_fp8_sdwa v[170:171], v170 src0_sel:WORD_1
	s_waitcnt vmcnt(1)
	v_cvt_pk_f32_fp8_e32 v[172:173], v174
	v_cvt_pk_f32_fp8_sdwa v[174:175], v174 src0_sel:WORD_1
	s_waitcnt vmcnt(0)
; __device__ __forceinline__ float bflo(unsigned w) { return __uint_as_float(w << 16); }
; __device__ __forceinline__ float bfhi(unsigned w) { return __uint_as_float(w & 0xffff0000u); }
; __global__ void __launch_bounds__(512, 2) mega_fwd(Args args) {
;     ...
;             for (int j = 0; j < 8; ++j) { const u32x2 h_ = hr[64 * j]; v[j] = (f32x4){bflo(h_.x), bfhi(h_.x), bflo(h_.y), bfhi(h_.y)}; }
; #pragma unroll
;             for (int k = 0; k < 4; ++k) { const int dest = tab[AE[m * 4 + k]] + AP[m * 4 + k]; const float w = AW[m * 4 + k] * 0.125f; const int* yr = (const int*)(YY + (size_t)dest * DM) + ln;
; #pragma unroll
;                 for (int j = 0; j < 8; ++j) { const int y = yr[64 * j]; const f32x2 ylo = __builtin_amdgcn_cvt_pk_f32_fp8(y, false), yhi = __builtin_amdgcn_cvt_pk_f32_fp8(y, true);
;                     v[j][0] += w * ylo.x; v[j][1] += w * ylo.y; v[j][2] += w * yhi.x; v[j][3] += w * yhi.y; } }
	v_cvt_pk_f32_fp8_e32 v[176:177], v178
	v_cvt_pk_f32_fp8_sdwa v[178:179], v178 src0_sel:WORD_1
	v_mov_b32_e32 v80, v44
	v_mov_b32_e32 v82, v40
	v_mov_b32_e32 v40, v46
	v_mov_b32_e32 v44, v50
	v_mov_b32_e32 v81, v78
	v_mov_b32_e32 v83, v76
	v_mov_b32_e32 v76, v41
	v_mov_b32_e32 v78, v45
	v_mov_b32_e32 v41, v84
	v_mov_b32_e32 v84, v47
	v_mov_b32_e32 v45, v86
	v_mov_b32_e32 v86, v51
	v_mov_b32_e32 v46, v52
	v_mov_b32_e32 v50, v54
	v_mov_b32_e32 v52, v56
	v_mov_b32_e32 v54, v58
	v_mov_b32_e32 v56, v60
	v_mov_b32_e32 v58, v62
	v_mov_b32_e32 v60, v64
	v_mov_b32_e32 v62, v66
	v_mov_b32_e32 v64, v68
	v_mov_b32_e32 v66, v70
	v_mov_b32_e32 v68, v72
	v_mov_b32_e32 v70, v74
	v_mov_b32_e32 v47, v88
	v_mov_b32_e32 v88, v53
	v_mov_b32_e32 v51, v90
	v_mov_b32_e32 v90, v55
	v_mov_b32_e32 v53, v92
	v_mov_b32_e32 v92, v57
	v_mov_b32_e32 v55, v94
	v_mov_b32_e32 v94, v59
	v_mov_b32_e32 v57, v96
	v_mov_b32_e32 v96, v61
	v_mov_b32_e32 v59, v98
	v_mov_b32_e32 v98, v63
	v_mov_b32_e32 v61, v100
	v_mov_b32_e32 v100, v65
	v_mov_b32_e32 v63, v102
	v_mov_b32_e32 v102, v67
	v_mov_b32_e32 v65, v104
	v_mov_b32_e32 v104, v69
	v_mov_b32_e32 v67, v106
	v_mov_b32_e32 v106, v71
	v_mov_b32_e32 v69, v108
	v_mov_b32_e32 v108, v73
	v_mov_b32_e32 v71, v110
	v_mov_b32_e32 v110, v75
	v_pk_mul_f32 v[80:81], v[48:49], v[80:81]
	v_pk_mul_f32 v[82:83], v[48:49], v[82:83]
	v_pk_mul_f32 v[76:77], v[48:49], v[76:77]
	v_pk_mul_f32 v[78:79], v[48:49], v[78:79]
	v_pk_mul_f32 v[40:41], v[48:49], v[40:41]
	v_pk_mul_f32 v[84:85], v[48:49], v[84:85]
	v_pk_mul_f32 v[44:45], v[48:49], v[44:45]
	v_pk_mul_f32 v[86:87], v[48:49], v[86:87]
	v_pk_mul_f32 v[42:43], v[42:43], s[30:31] op_sel_hi:[1,0]
	v_mov_b32_e32 v72, v114
	v_mov_b32_e32 v73, v146
	v_mov_b32_e32 v74, v112
	v_mov_b32_e32 v75, v144
	v_mov_b32_e32 v144, v113
	v_mov_b32_e32 v146, v115
	v_mov_b32_e32 v113, v148
	v_mov_b32_e32 v148, v117
	v_mov_b32_e32 v115, v150
	v_mov_b32_e32 v150, v119
	v_pk_mul_f32 v[46:47], v[48:49], v[46:47]
	v_pk_mul_f32 v[88:89], v[48:49], v[88:89]
	v_pk_mul_f32 v[50:51], v[48:49], v[50:51]
	v_pk_mul_f32 v[90:91], v[48:49], v[90:91]
	v_pk_mul_f32 v[52:53], v[48:49], v[52:53]
	v_pk_mul_f32 v[92:93], v[48:49], v[92:93]
	v_pk_mul_f32 v[54:55], v[48:49], v[54:55]
	v_pk_mul_f32 v[94:95], v[48:49], v[94:95]
	v_pk_mul_f32 v[56:57], v[48:49], v[56:57]
	v_pk_mul_f32 v[96:97], v[48:49], v[96:97]
	v_pk_mul_f32 v[58:59], v[48:49], v[58:59]
	v_pk_mul_f32 v[98:99], v[48:49], v[98:99]
	v_pk_mul_f32 v[60:61], v[48:49], v[60:61]
	v_pk_mul_f32 v[100:101], v[48:49], v[100:101]
	v_pk_mul_f32 v[62:63], v[48:49], v[62:63]
	v_pk_mul_f32 v[102:103], v[48:49], v[102:103]
	v_pk_mul_f32 v[64:65], v[48:49], v[64:65]
	v_pk_mul_f32 v[104:105], v[48:49], v[104:105]
	v_pk_mul_f32 v[66:67], v[48:49], v[66:67]
	v_pk_mul_f32 v[106:107], v[48:49], v[106:107]
	v_pk_mul_f32 v[68:69], v[48:49], v[68:69]
	v_pk_mul_f32 v[108:109], v[48:49], v[108:109]
	v_pk_mul_f32 v[70:71], v[48:49], v[70:71]
	v_pk_mul_f32 v[48:49], v[48:49], v[110:111]
	v_add_f32_e32 v39, v80, v180
	v_add_f32_e32 v80, v82, v165
	v_add_f32_e32 v76, v76, v167
	v_add_f32_e32 v78, v78, v181
	v_add_f32_e32 v40, v40, v182
	v_add_f32_e32 v82, v84, v183
	v_add_f32_e32 v44, v44, v184
	v_add_f32_e32 v84, v86, v185
	v_mov_b32_e32 v112, v116
	v_mov_b32_e32 v114, v118
	v_mov_b32_e32 v116, v120
	v_mov_b32_e32 v117, v152
	v_mov_b32_e32 v152, v121
	v_mov_b32_e32 v118, v122
	v_mov_b32_e32 v119, v154
	v_mov_b32_e32 v154, v123
	v_mov_b32_e32 v120, v124
	v_mov_b32_e32 v121, v156
	v_mov_b32_e32 v156, v125
	v_mov_b32_e32 v122, v126
	v_mov_b32_e32 v123, v158
	v_mov_b32_e32 v158, v127
	v_mov_b32_e32 v124, v128
	v_mov_b32_e32 v125, v160
	v_mov_b32_e32 v160, v129
	v_mov_b32_e32 v126, v130
	v_mov_b32_e32 v127, v162
	v_mov_b32_e32 v162, v131
	v_mov_b32_e32 v128, v132
	v_mov_b32_e32 v129, v168
	v_mov_b32_e32 v168, v133
	v_mov_b32_e32 v130, v134
	v_mov_b32_e32 v131, v170
	v_mov_b32_e32 v170, v135
	v_mov_b32_e32 v132, v136
	v_mov_b32_e32 v133, v172
	v_mov_b32_e32 v172, v137
	v_mov_b32_e32 v134, v138
	v_mov_b32_e32 v135, v174
	v_mov_b32_e32 v174, v139
	v_mov_b32_e32 v136, v140
	v_mov_b32_e32 v137, v176
	v_mov_b32_e32 v176, v141
	v_mov_b32_e32 v138, v142
	v_mov_b32_e32 v139, v178
	v_mov_b32_e32 v178, v143
	v_pk_mul_f32 v[72:73], v[42:43], v[72:73]
	v_pk_mul_f32 v[74:75], v[42:43], v[74:75]
	v_pk_mul_f32 v[110:111], v[42:43], v[144:145]
	v_pk_mul_f32 v[140:141], v[42:43], v[146:147]
	v_pk_mul_f32 v[142:143], v[42:43], v[148:149]
	v_pk_mul_f32 v[144:145], v[42:43], v[150:151]
	v_add_f32_e32 v46, v46, v186
	v_add_f32_e32 v86, v88, v187
	v_add_f32_e32 v50, v50, v188
	v_add_f32_e32 v88, v90, v189
	v_add_f32_e32 v70, v70, v208
	v_add_f32_e32 v48, v48, v209
	v_add_f32_e32 v80, v83, v80
	v_add_f32_e32 v76, v77, v76
	v_add_f32_e32 v39, v39, v81
	v_add_f32_e32 v77, v78, v79
	v_add_f32_e32 v40, v41, v40
	v_add_f32_e32 v41, v85, v82
	v_add_f32_e32 v44, v44, v45
	v_add_f32_e32 v45, v84, v87
	v_pk_mul_f32 v[112:113], v[42:43], v[112:113]
	v_pk_mul_f32 v[114:115], v[42:43], v[114:115]
	v_pk_mul_f32 v[116:117], v[42:43], v[116:117]
	v_pk_mul_f32 v[146:147], v[42:43], v[152:153]
	v_pk_mul_f32 v[118:119], v[42:43], v[118:119]
	v_pk_mul_f32 v[148:149], v[42:43], v[154:155]
	v_pk_mul_f32 v[120:121], v[42:43], v[120:121]
	v_pk_mul_f32 v[150:151], v[42:43], v[156:157]
	v_pk_mul_f32 v[122:123], v[42:43], v[122:123]
	v_pk_mul_f32 v[152:153], v[42:43], v[158:159]
	v_pk_mul_f32 v[124:125], v[42:43], v[124:125]
	v_pk_mul_f32 v[154:155], v[42:43], v[160:161]
	v_pk_mul_f32 v[126:127], v[42:43], v[126:127]
	v_pk_mul_f32 v[156:157], v[42:43], v[162:163]
	v_pk_mul_f32 v[128:129], v[42:43], v[128:129]
	v_pk_mul_f32 v[158:159], v[42:43], v[168:169]
; __device__ __forceinline__ unsigned cvtpk(float lo, float hi) { unsigned r; asm volatile("v_cvt_pk_bf16_f32 %0, %1, %2" : "=v"(r) : "v"(lo), "v"(hi)); return r; }
; __global__ void __launch_bounds__(512, 2) mega_fwd(Args args) {
;     ...
;                     v[j][0] += w * ylo.x; v[j][1] += w * ylo.y; v[j][2] += w * yhi.x; v[j][3] += w * yhi.y; } }
;             float s = 0.f;
; #pragma unroll
;             for (int j = 0; j < 8; ++j) { u32x2 hw_; hw_.x = cvtpk(v[j][0], v[j][1]); hw_.y = cvtpk(v[j][2], v[j][3]); hr[64 * j] = hw_; s += (v[j][0] * v[j][0] + v[j][1] * v[j][1]) + (v[j][2] * v[j][2] + v[j][3] * v[j][3]); }
	v_pk_mul_f32 v[130:131], v[42:43], v[130:131]
	v_pk_mul_f32 v[160:161], v[42:43], v[170:171]
	v_pk_mul_f32 v[132:133], v[42:43], v[132:133]
	v_pk_mul_f32 v[162:163], v[42:43], v[172:173]
	v_pk_mul_f32 v[134:135], v[42:43], v[134:135]
	v_pk_mul_f32 v[168:169], v[42:43], v[174:175]
	v_pk_mul_f32 v[136:137], v[42:43], v[136:137]
	v_pk_mul_f32 v[170:171], v[42:43], v[176:177]
	v_pk_mul_f32 v[138:139], v[42:43], v[138:139]
	v_pk_mul_f32 v[42:43], v[42:43], v[178:179]
	v_add_f32_e32 v52, v52, v190
	v_add_f32_e32 v90, v92, v191
	v_add_f32_e32 v54, v54, v192
	v_add_f32_e32 v92, v94, v193
	v_add_f32_e32 v46, v47, v46
	v_add_f32_e32 v47, v89, v86
	v_add_f32_e32 v50, v50, v51
	v_add_f32_e32 v51, v88, v91
	v_add_f32_e32 v70, v70, v71
	v_add_f32_e32 v48, v48, v49
	v_add_f32_e32 v39, v39, v72
	v_add_f32_e32 v49, v74, v80
	v_add_f32_e32 v71, v110, v76
	v_add_f32_e32 v72, v77, v140
	v_add_f32_e32 v41, v142, v41
	v_add_f32_e32 v45, v45, v144
	v_add_f32_e32 v56, v56, v194
	v_add_f32_e32 v94, v96, v195
	v_add_f32_e32 v58, v58, v196
	v_add_f32_e32 v96, v98, v197
	v_add_f32_e32 v52, v53, v52
	v_add_f32_e32 v53, v93, v90
	v_add_f32_e32 v54, v54, v55
	v_add_f32_e32 v55, v92, v95
	v_add_f32_e32 v40, v112, v40
	v_add_f32_e32 v44, v44, v114
	v_add_f32_e32 v47, v146, v47
	v_add_f32_e32 v51, v51, v148
	v_add_f32_e32 v42, v48, v42
	v_add_f32_e32 v48, v75, v49
	v_add_f32_e32 v49, v111, v71
	v_add_f32_e32 v39, v39, v73
	v_add_f32_e32 v71, v72, v141
	v_add_f32_e32 v73, v143, v41
	v_add_f32_e32 v45, v45, v145
	v_add_f32_e32 v60, v60, v198
	v_add_f32_e32 v98, v100, v199
	v_add_f32_e32 v62, v62, v200
	v_add_f32_e32 v100, v102, v201
	v_add_f32_e32 v56, v57, v56
	v_add_f32_e32 v57, v97, v94
	v_add_f32_e32 v58, v58, v59
	v_add_f32_e32 v59, v96, v99
	v_add_f32_e32 v46, v116, v46
	v_add_f32_e32 v50, v50, v118
	v_add_f32_e32 v53, v150, v53
	v_add_f32_e32 v55, v55, v152
	v_add_f32_e32 v72, v113, v40
	v_add_f32_e32 v44, v44, v115
	v_add_f32_e32 v47, v147, v47
	v_add_f32_e32 v51, v51, v149
	v_add_f32_e32 v74, v42, v43
	v_cvt_pk_bf16_f32 v40, v48, v49
	v_cvt_pk_bf16_f32 v41, v39, v71
	v_mul_f32_e32 v42, v49, v49
	v_mul_f32_e32 v43, v71, v71
	v_mul_f32_e32 v75, v73, v73
	v_mul_f32_e32 v76, v45, v45
	v_add_f32_e32 v64, v64, v202
	v_add_f32_e32 v102, v104, v203
	v_add_f32_e32 v66, v66, v204
	v_add_f32_e32 v104, v106, v205
	v_add_f32_e32 v60, v61, v60
	v_add_f32_e32 v61, v101, v98
	v_add_f32_e32 v62, v62, v63
	v_add_f32_e32 v63, v100, v103
	v_add_f32_e32 v52, v120, v52
	v_add_f32_e32 v54, v54, v122
	v_add_f32_e32 v57, v154, v57
	v_add_f32_e32 v59, v59, v156
	v_add_f32_e32 v46, v117, v46
	v_add_f32_e32 v50, v50, v119
	v_add_f32_e32 v53, v151, v53
	v_add_f32_e32 v55, v55, v153
	v_mul_f32_e32 v77, v47, v47
	v_mul_f32_e32 v78, v51, v51
	global_store_dwordx2 v[18:19], v[40:41], off
	v_fmac_f32_e32 v42, v48, v48
	v_fmac_f32_e32 v43, v39, v39
	v_cvt_pk_bf16_f32 v40, v72, v73
	v_cvt_pk_bf16_f32 v41, v44, v45
	v_fmac_f32_e32 v75, v72, v72
	v_fmac_f32_e32 v76, v44, v44
	v_add_f32_e32 v64, v65, v64
	v_add_f32_e32 v65, v105, v102
	v_add_f32_e32 v66, v66, v67
	v_add_f32_e32 v67, v104, v107
	v_add_f32_e32 v56, v124, v56
	v_add_f32_e32 v58, v58, v126
	v_add_f32_e32 v61, v158, v61
	v_add_f32_e32 v63, v63, v160
	v_add_f32_e32 v52, v121, v52
	v_add_f32_e32 v54, v54, v123
	v_add_f32_e32 v57, v155, v57
	v_add_f32_e32 v59, v59, v157
	v_mul_f32_e32 v79, v53, v53
	v_mul_f32_e32 v80, v55, v55
	v_fmac_f32_e32 v77, v46, v46
	v_fmac_f32_e32 v78, v50, v50
	v_add_f32_e32 v42, v42, v43
	global_store_dwordx2 v[18:19], v[40:41], off offset:512
	v_add_f32_e32 v43, v75, v76
	v_cvt_pk_bf16_f32 v40, v46, v47
	v_cvt_pk_bf16_f32 v41, v50, v51
	v_add_f32_e32 v60, v128, v60
	v_add_f32_e32 v62, v62, v130
	v_add_f32_e32 v65, v162, v65
	v_add_f32_e32 v67, v67, v168
	v_add_f32_e32 v56, v125, v56
	v_add_f32_e32 v58, v58, v127
	v_add_f32_e32 v61, v159, v61
	v_add_f32_e32 v63, v63, v161
	v_mul_f32_e32 v81, v57, v57
	v_mul_f32_e32 v82, v59, v59
	v_fmac_f32_e32 v79, v52, v52
	v_fmac_f32_e32 v80, v54, v54
	v_add_f32_e32 v75, v77, v78
	v_add_f32_e32 v42, v42, v43
	global_store_dwordx2 v[18:19], v[40:41], off offset:1024
	v_cvt_pk_bf16_f32 v40, v52, v53
	v_cvt_pk_bf16_f32 v41, v54, v55
	v_add_f32_e32 v68, v68, v206
	v_add_f32_e32 v106, v108, v207
	v_add_f32_e32 v64, v132, v64
	v_add_f32_e32 v66, v66, v134
	v_add_f32_e32 v60, v129, v60
	v_add_f32_e32 v62, v62, v131
	v_add_f32_e32 v65, v163, v65
	v_add_f32_e32 v67, v67, v169
	v_mul_f32_e32 v83, v61, v61
	v_mul_f32_e32 v84, v63, v63
	v_fmac_f32_e32 v81, v56, v56
	v_fmac_f32_e32 v82, v58, v58
	v_add_f32_e32 v76, v79, v80
	v_add_f32_e32 v42, v42, v75
	global_store_dwordx2 v[18:19], v[40:41], off offset:1536
	v_cvt_pk_bf16_f32 v40, v56, v57
	v_cvt_pk_bf16_f32 v41, v58, v59
	v_add_f32_e32 v68, v69, v68
	v_add_f32_e32 v69, v109, v106
	v_add_f32_e32 v64, v133, v64
	v_add_f32_e32 v66, v66, v135
	v_mul_f32_e32 v85, v65, v65
	v_mul_f32_e32 v86, v67, v67
	v_fmac_f32_e32 v83, v60, v60
	v_fmac_f32_e32 v84, v62, v62
	v_add_f32_e32 v77, v81, v82
	v_add_f32_e32 v42, v42, v76
	global_store_dwordx2 v[18:19], v[40:41], off offset:2048
	v_cvt_pk_bf16_f32 v40, v60, v61
	v_cvt_pk_bf16_f32 v41, v62, v63
	v_add_f32_e32 v68, v136, v68
	v_add_f32_e32 v69, v170, v69
	v_add_f32_e32 v70, v70, v138
	v_fmac_f32_e32 v85, v64, v64
	v_fmac_f32_e32 v86, v66, v66
	v_add_f32_e32 v78, v83, v84
	v_add_f32_e32 v42, v42, v77
	global_store_dwordx2 v[18:19], v[40:41], off offset:2560
	v_cvt_pk_bf16_f32 v40, v64, v65
	v_cvt_pk_bf16_f32 v41, v66, v67
	v_add_f32_e32 v68, v137, v68
	v_add_f32_e32 v69, v171, v69
	v_add_f32_e32 v70, v70, v139
	v_add_f32_e32 v79, v85, v86
	v_add_f32_e32 v42, v42, v78
	global_store_dwordx2 v[18:19], v[40:41], off offset:3072
	v_cvt_pk_bf16_f32 v40, v68, v69
	v_cvt_pk_bf16_f32 v41, v70, v74
	global_store_dwordx2 v[18:19], v[40:41], off offset:3584
	v_add_f32_e32 v75, v42, v79
	global_load_dwordx4 v[40:43], v[4:5], off
	v_mul_f32_e32 v87, v69, v69
	v_mul_f32_e32 v88, v74, v74
	v_fmac_f32_e32 v87, v68, v68
	v_fmac_f32_e32 v88, v70, v70
	v_add_f32_e32 v80, v87, v88
	v_add_f32_e32 v18, v75, v80
	ds_bpermute_b32 v19, v38, v18
	s_waitcnt lgkmcnt(0)
; __device__ __forceinline__ unsigned cvt4_fp8(float a, float b, float c, float d) { int w = 0; w = __builtin_amdgcn_cvt_pk_fp8_f32(a, b, w, false); w = __builtin_amdgcn_cvt_pk_fp8_f32(c, d, w, true); return (unsigned)w; }
; __global__ void __launch_bounds__(512, 2) mega_fwd(Args args) {
;     ...
;             const float rstd = 1.0f / sqrtf(wave_sum(s) * (1.0f / DM) + EPS);
;             unsigned* o4 = (unsigned*)(XN8 + (size_t)m * DM) + ln;
; #pragma unroll
;             for (int j = 0; j < 8; ++j) { const f32x4 gv = ((const f32x4*)gn)[64 * j + ln]; o4[64 * j] = cvt4_fp8(v[j][0] * rstd * gv[0], v[j][1] * rstd * gv[1], v[j][2] * rstd * gv[2], v[j][3] * rstd * gv[3]); } }
	v_add_f32_e32 v18, v18, v19
	ds_bpermute_b32 v19, v37, v18
	s_waitcnt lgkmcnt(0)
	v_add_f32_e32 v18, v18, v19
	ds_bpermute_b32 v19, v36, v18
	s_waitcnt lgkmcnt(0)
	v_add_f32_e32 v18, v18, v19
	ds_bpermute_b32 v19, v35, v18
	s_waitcnt lgkmcnt(0)
	v_add_f32_e32 v18, v18, v19
	ds_bpermute_b32 v19, v34, v18
	s_waitcnt lgkmcnt(0)
	v_add_f32_e32 v18, v18, v19
	ds_bpermute_b32 v19, v33, v18
	s_waitcnt lgkmcnt(0)
	v_add_f32_e32 v18, v18, v19
	v_fmamk_f32 v18, v18, 0x3a000000, v30
	v_mul_f32_e32 v19, 0x4f800000, v18
	v_cmp_gt_f32_e32 vcc, s11, v18
	s_nop 1
	v_cndmask_b32_e32 v18, v18, v19, vcc
	v_sqrt_f32_e32 v19, v18
	s_nop 0
	v_add_u32_e32 v33, -1, v19
	v_add_u32_e32 v34, 1, v19
	v_fma_f32 v35, -v33, v19, v18
	v_fma_f32 v36, -v34, v19, v18
	v_cmp_ge_f32_e64 s[4:5], 0, v35
	s_nop 1
	v_cndmask_b32_e64 v19, v19, v33, s[4:5]
	v_cmp_lt_f32_e64 s[4:5], 0, v36
	s_nop 1
	v_cndmask_b32_e64 v19, v19, v34, s[4:5]
	v_mul_f32_e32 v33, 0x37800000, v19
	v_cndmask_b32_e32 v19, v19, v33, vcc
	v_cmp_class_f32_e32 vcc, v18, v31
	s_nop 1
	v_cndmask_b32_e32 v18, v19, v18, vcc
	v_div_scale_f32 v19, s[4:5], v18, v18, 1.0
	v_rcp_f32_e32 v34, v19
	v_div_scale_f32 v33, vcc, 1.0, v18, 1.0
	v_fma_f32 v35, -v19, v34, 1.0
	v_fmac_f32_e32 v34, v35, v34
	v_mul_f32_e32 v35, v33, v34
	v_fma_f32 v36, -v19, v35, v33
	v_fmac_f32_e32 v35, v36, v34
	v_fma_f32 v19, -v19, v35, v33
	v_div_fmas_f32 v19, v19, v34, v35
	v_div_fixup_f32 v18, v19, v18, 1.0
	v_mul_f32_e32 v19, v18, v48
	v_mul_f32_e32 v33, v18, v49
	s_waitcnt vmcnt(0)
	v_mul_f32_e32 v19, v40, v19
	v_mul_f32_e32 v33, v41, v33
	v_cvt_pk_fp8_f32 v32, v19, v33
	v_mul_f32_e32 v34, v18, v39
	v_mul_f32_e32 v35, v18, v71
	v_mul_f32_e32 v34, v42, v34
	v_mul_f32_e32 v35, v43, v35
	v_cvt_pk_fp8_f32 v32, v34, v35 op_sel:[0,0,1]
	v_mul_f32_e32 v36, v18, v72
	v_mul_f32_e32 v37, v18, v73
	v_mov_b32_e32 v19, 0
	global_store_dword v[20:21], v32, off
	v_mul_f32_e32 v38, v18, v44
	v_mul_f32_e32 v39, v18, v45
	v_mov_b32_e32 v32, v212
	v_mov_b32_e32 v33, v213
	v_mov_b32_e32 v34, v214
	v_mov_b32_e32 v35, v215
	v_mul_f32_e32 v32, v32, v36
	v_mul_f32_e32 v33, v33, v37
	v_cvt_pk_fp8_f32 v19, v32, v33
	v_mul_f32_e32 v34, v34, v38
	v_mul_f32_e32 v35, v35, v39
	v_mul_f32_e32 v36, v18, v46
	v_cvt_pk_fp8_f32 v19, v34, v35 op_sel:[0,0,1]
	v_mul_f32_e32 v37, v18, v47
	v_mul_f32_e32 v38, v18, v50
	v_mul_f32_e32 v39, v18, v51
	global_store_dword v[20:21], v19, off offset:256
	v_mov_b32_e32 v19, 0
	v_mov_b32_e32 v32, v216
	v_mov_b32_e32 v33, v217
	v_mov_b32_e32 v34, v218
	v_mov_b32_e32 v35, v219
	v_mul_f32_e32 v32, v32, v36
	v_mul_f32_e32 v33, v33, v37
	v_cvt_pk_fp8_f32 v19, v32, v33
	v_mul_f32_e32 v34, v34, v38
	v_mul_f32_e32 v35, v35, v39
	v_mul_f32_e32 v36, v18, v52
	v_cvt_pk_fp8_f32 v19, v34, v35 op_sel:[0,0,1]
	v_mul_f32_e32 v37, v18, v53
	v_mul_f32_e32 v38, v18, v54
	v_mul_f32_e32 v39, v18, v55
	global_store_dword v[20:21], v19, off offset:512
	v_mov_b32_e32 v19, 0
	v_mov_b32_e32 v32, v220
	v_mov_b32_e32 v33, v221
	v_mov_b32_e32 v34, v222
	v_mov_b32_e32 v35, v223
	v_mul_f32_e32 v32, v32, v36
	v_mul_f32_e32 v33, v33, v37
	v_cvt_pk_fp8_f32 v19, v32, v33
	v_mul_f32_e32 v34, v34, v38
	v_mul_f32_e32 v35, v35, v39
	v_mul_f32_e32 v36, v18, v56
	v_cvt_pk_fp8_f32 v19, v34, v35 op_sel:[0,0,1]
	v_mul_f32_e32 v37, v18, v57
	v_mul_f32_e32 v38, v18, v58
	v_mul_f32_e32 v39, v18, v59
	global_store_dword v[20:21], v19, off offset:768
	v_mov_b32_e32 v19, 0
	v_mov_b32_e32 v32, v224
	v_mov_b32_e32 v33, v225
	v_mov_b32_e32 v34, v226
	v_mov_b32_e32 v35, v227
	v_mul_f32_e32 v32, v32, v36
	v_mul_f32_e32 v33, v33, v37
	v_cvt_pk_fp8_f32 v19, v32, v33
	v_mul_f32_e32 v34, v34, v38
	v_mul_f32_e32 v35, v35, v39
	v_mul_f32_e32 v36, v18, v60
	v_cvt_pk_fp8_f32 v19, v34, v35 op_sel:[0,0,1]
	v_mul_f32_e32 v37, v18, v61
	v_mul_f32_e32 v38, v18, v62
	v_mul_f32_e32 v39, v18, v63
	global_store_dword v[20:21], v19, off offset:1024
	v_mov_b32_e32 v19, 0
	v_mov_b32_e32 v32, v228
	v_mov_b32_e32 v33, v229
	v_mov_b32_e32 v34, v230
	v_mov_b32_e32 v35, v231
	v_mul_f32_e32 v32, v32, v36
	v_mul_f32_e32 v33, v33, v37
	v_cvt_pk_fp8_f32 v19, v32, v33
	v_mul_f32_e32 v34, v34, v38
	v_mul_f32_e32 v32, v35, v39
	v_mul_f32_e32 v36, v18, v64
	v_cvt_pk_fp8_f32 v19, v34, v32 op_sel:[0,0,1]
	v_mul_f32_e32 v37, v18, v65
	v_mul_f32_e32 v38, v18, v66
	v_mul_f32_e32 v39, v18, v67
	global_store_dword v[20:21], v19, off offset:1280
	v_mov_b32_e32 v19, 0
	v_mov_b32_e32 v32, v232
	v_mov_b32_e32 v33, v233
	v_mov_b32_e32 v34, v234
	v_mov_b32_e32 v35, v235
	v_mul_f32_e32 v32, v32, v36
	v_mul_f32_e32 v33, v33, v37
	v_cvt_pk_fp8_f32 v19, v32, v33
	v_mul_f32_e32 v32, v34, v38
	v_mul_f32_e32 v33, v35, v39
	v_mul_f32_e32 v36, v18, v68
	v_cvt_pk_fp8_f32 v19, v32, v33 op_sel:[0,0,1]
	v_mul_f32_e32 v37, v18, v69
	v_mul_f32_e32 v38, v18, v70
	v_mul_f32_e32 v18, v18, v74
	global_store_dword v[20:21], v19, off offset:1536
	v_mov_b32_e32 v19, 0
	v_mov_b32_e32 v32, v236
	v_mov_b32_e32 v33, v237
	v_mov_b32_e32 v34, v238
	v_mov_b32_e32 v35, v239
	v_mul_f32_e32 v32, v32, v36
	v_mul_f32_e32 v33, v33, v37
	v_cvt_pk_fp8_f32 v19, v32, v33
	v_mul_f32_e32 v32, v34, v38
	v_mul_f32_e32 v18, v35, v18
	v_cvt_pk_fp8_f32 v19, v32, v18 op_sel:[0,0,1]
	global_store_dword v[20:21], v19, off offset:1792
	s_cbranch_scc1 .LBB0_2656
